# GEMM K-loops: priority yield point every 2 fp8 MFMAs / every 4 bf16 MFMAs (on top of v34)
# baseline (speedup 1.0000x reference)
.LBB0_290:
	s_add_u32 s46, s44, 0xfffc0080
	s_addc_u32 s47, s45, -1
	s_add_i32 s62, 0, 0x10000
	s_cmp_eq_u32 s61, 12
	s_cselect_b32 s49, s1, s47
	s_cselect_b32 s48, s5, s46
	s_cselect_b32 s47, s35, s60
	s_cselect_b32 s46, s37, s59
	s_add_i32 s64, 0, 0x14000
	v_add_u32_e32 v158, s62, v148
	v_add_u32_e32 v174, s64, v148
	ds_read_b128 v[144:147], v158
	ds_read_b128 v[150:153], v158 offset:1024
	ds_read_b128 v[154:157], v158 offset:2048
	ds_read_b128 v[158:161], v158 offset:3072
	ds_read_b128 v[162:165], v174
	ds_read_b128 v[166:169], v174 offset:1024
	ds_read_b128 v[170:173], v174 offset:2048
	ds_read_b128 v[174:177], v174 offset:3072
	v_lshl_add_u64 v[210:211], s[44:45], 0, v[140:141]
	s_add_i32 m0, s50, 0xc000
	ds_read_b128 v[178:181], v149
	ds_read_b128 v[182:185], v149 offset:1024
	ds_read_b128 v[186:189], v149 offset:2048
	ds_read_b128 v[190:193], v149 offset:3072
	ds_read_b128 v[194:197], v149 offset:4096
	ds_read_b128 v[198:201], v149 offset:5120
	ds_read_b128 v[202:205], v149 offset:6144
	ds_read_b128 v[206:209], v149 offset:7168
	global_load_lds_dwordx4 v[210:211], off
	v_lshl_add_u64 v[210:211], s[44:45], 0, v[142:143]
	s_add_i32 m0, s50, 0xe000
	s_nop 0
	global_load_lds_dwordx4 v[210:211], off
	s_waitcnt vmcnt(8)
	s_waitcnt lgkmcnt(0)
	s_barrier
	s_setprio 1
	s_waitcnt lgkmcnt(0)
	v_mfma_f32_16x16x32_bf16 v[130:133], v[144:147], v[178:181], v[130:133]
	v_mfma_f32_16x16x32_bf16 v[126:129], v[154:157], v[178:181], v[126:129]
	v_mfma_f32_16x16x32_bf16 v[114:117], v[144:147], v[186:189], v[114:117]
	v_mfma_f32_16x16x32_bf16 v[110:113], v[154:157], v[186:189], v[110:113]
	s_setprio 0
	s_setprio 1
	v_mfma_f32_16x16x32_bf16 v[98:101], v[144:147], v[194:197], v[98:101]
	v_mfma_f32_16x16x32_bf16 v[94:97], v[154:157], v[194:197], v[94:97]
	v_mfma_f32_16x16x32_bf16 v[82:85], v[144:147], v[202:205], v[82:85]
	v_mfma_f32_16x16x32_bf16 v[78:81], v[154:157], v[202:205], v[78:81]
	s_setprio 0
	s_setprio 1
	v_mfma_f32_16x16x32_bf16 v[130:133], v[150:153], v[182:185], v[130:133]
	v_mfma_f32_16x16x32_bf16 v[126:129], v[158:161], v[182:185], v[126:129]
	v_mfma_f32_16x16x32_bf16 v[114:117], v[150:153], v[190:193], v[114:117]
	v_mfma_f32_16x16x32_bf16 v[110:113], v[158:161], v[190:193], v[110:113]
	s_setprio 0
	s_setprio 1
	v_mfma_f32_16x16x32_bf16 v[98:101], v[150:153], v[198:201], v[98:101]
	v_mfma_f32_16x16x32_bf16 v[94:97], v[158:161], v[198:201], v[94:97]
	v_mfma_f32_16x16x32_bf16 v[82:85], v[150:153], v[206:209], v[82:85]
	v_mfma_f32_16x16x32_bf16 v[78:81], v[158:161], v[206:209], v[78:81]
	s_setprio 0
	s_setprio 1
	v_mfma_f32_16x16x32_bf16 v[122:125], v[162:165], v[178:181], v[122:125]
	v_mfma_f32_16x16x32_bf16 v[118:121], v[170:173], v[178:181], v[118:121]
	v_mfma_f32_16x16x32_bf16 v[106:109], v[162:165], v[186:189], v[106:109]
	v_mfma_f32_16x16x32_bf16 v[102:105], v[170:173], v[186:189], v[102:105]
	s_setprio 0
	s_setprio 1
	v_mfma_f32_16x16x32_bf16 v[90:93], v[162:165], v[194:197], v[90:93]
	v_mfma_f32_16x16x32_bf16 v[86:89], v[170:173], v[194:197], v[86:89]
	v_mfma_f32_16x16x32_bf16 v[74:77], v[162:165], v[202:205], v[74:77]
	v_mfma_f32_16x16x32_bf16 v[70:73], v[170:173], v[202:205], v[70:73]
	s_setprio 0
	s_setprio 1
	v_mfma_f32_16x16x32_bf16 v[122:125], v[166:169], v[182:185], v[122:125]
	v_mfma_f32_16x16x32_bf16 v[118:121], v[174:177], v[182:185], v[118:121]
	v_mfma_f32_16x16x32_bf16 v[106:109], v[166:169], v[190:193], v[106:109]
	v_mfma_f32_16x16x32_bf16 v[102:105], v[174:177], v[190:193], v[102:105]
	s_setprio 0
	s_setprio 1
	v_mfma_f32_16x16x32_bf16 v[90:93], v[166:169], v[198:201], v[90:93]
	v_mfma_f32_16x16x32_bf16 v[86:89], v[174:177], v[198:201], v[86:89]
	v_mfma_f32_16x16x32_bf16 v[74:77], v[166:169], v[206:209], v[74:77]
	v_mfma_f32_16x16x32_bf16 v[70:73], v[174:177], v[206:209], v[70:73]
	s_setprio 0
	s_barrier
	s_add_i32 s62, s62, s27
	v_lshl_add_u64 v[210:211], s[46:47], 0, v[0:1]
	s_mov_b32 m0, s62
	ds_read_b128 v[178:181], v149 offset:16384
	ds_read_b128 v[182:185], v149 offset:17408
	ds_read_b128 v[186:189], v149 offset:18432
	ds_read_b128 v[190:193], v149 offset:19456
	ds_read_b128 v[194:197], v149 offset:20480
	ds_read_b128 v[198:201], v149 offset:21504
	ds_read_b128 v[202:205], v149 offset:22528
	ds_read_b128 v[206:209], v149 offset:23552
	global_load_lds_dwordx4 v[210:211], off
	s_add_i32 m0, s62, 0x2000
	s_add_u32 s62, s46, 0x40000
	v_lshl_add_u64 v[212:213], s[46:47], 0, v[138:139]
	s_addc_u32 s63, s47, 0
	s_add_i32 s64, s64, s27
	global_load_lds_dwordx4 v[212:213], off
	v_lshl_add_u64 v[216:217], s[62:63], 0, v[0:1]
	s_mov_b32 m0, s64
	v_lshl_add_u64 v[218:219], s[48:49], 0, v[136:137]
	global_load_lds_dwordx4 v[216:217], off
	v_lshl_add_u64 v[216:217], s[62:63], 0, v[138:139]
	s_add_i32 m0, s64, 0x2000
	s_nop 0
	global_load_lds_dwordx4 v[216:217], off
	v_lshl_add_u64 v[216:217], s[48:49], 0, v[134:135]
	s_mov_b32 m0, s50
	s_nop 0
	global_load_lds_dwordx4 v[216:217], off
	s_mov_b32 m0, s51
	s_nop 0
	global_load_lds_dwordx4 v[218:219], off
	s_waitcnt vmcnt(8)
	s_waitcnt lgkmcnt(0)
	s_barrier
	s_setprio 1
	s_waitcnt lgkmcnt(0)
	v_mfma_f32_16x16x32_bf16 v[66:69], v[144:147], v[178:181], v[66:69]
	v_mfma_f32_16x16x32_bf16 v[62:65], v[154:157], v[178:181], v[62:65]
	v_mfma_f32_16x16x32_bf16 v[50:53], v[144:147], v[186:189], v[50:53]
	v_mfma_f32_16x16x32_bf16 v[46:49], v[154:157], v[186:189], v[46:49]
	s_setprio 0
	s_setprio 1
	v_mfma_f32_16x16x32_bf16 v[34:37], v[144:147], v[194:197], v[34:37]
	v_mfma_f32_16x16x32_bf16 v[30:33], v[154:157], v[194:197], v[30:33]
	v_mfma_f32_16x16x32_bf16 v[18:21], v[144:147], v[202:205], v[18:21]
	v_mfma_f32_16x16x32_bf16 v[14:17], v[154:157], v[202:205], v[14:17]
	s_setprio 0
	s_setprio 1
	v_mfma_f32_16x16x32_bf16 v[66:69], v[150:153], v[182:185], v[66:69]
	v_mfma_f32_16x16x32_bf16 v[62:65], v[158:161], v[182:185], v[62:65]
	v_mfma_f32_16x16x32_bf16 v[50:53], v[150:153], v[190:193], v[50:53]
	v_mfma_f32_16x16x32_bf16 v[46:49], v[158:161], v[190:193], v[46:49]
	s_setprio 0
	s_setprio 1
	v_mfma_f32_16x16x32_bf16 v[34:37], v[150:153], v[198:201], v[34:37]
	v_mfma_f32_16x16x32_bf16 v[30:33], v[158:161], v[198:201], v[30:33]
	v_mfma_f32_16x16x32_bf16 v[18:21], v[150:153], v[206:209], v[18:21]
	v_mfma_f32_16x16x32_bf16 v[14:17], v[158:161], v[206:209], v[14:17]
	s_setprio 0
	s_setprio 1
	v_mfma_f32_16x16x32_bf16 v[58:61], v[162:165], v[178:181], v[58:61]
	v_mfma_f32_16x16x32_bf16 v[54:57], v[170:173], v[178:181], v[54:57]
	v_mfma_f32_16x16x32_bf16 v[42:45], v[162:165], v[186:189], v[42:45]
	v_mfma_f32_16x16x32_bf16 v[38:41], v[170:173], v[186:189], v[38:41]
	s_setprio 0
	s_setprio 1
	v_mfma_f32_16x16x32_bf16 v[26:29], v[162:165], v[194:197], v[26:29]
	v_mfma_f32_16x16x32_bf16 v[22:25], v[170:173], v[194:197], v[22:25]
	v_mfma_f32_16x16x32_bf16 v[10:13], v[162:165], v[202:205], v[10:13]
	v_mfma_f32_16x16x32_bf16 v[6:9], v[170:173], v[202:205], v[6:9]
	s_setprio 0
	s_setprio 1
	v_mfma_f32_16x16x32_bf16 v[58:61], v[166:169], v[182:185], v[58:61]
	v_mfma_f32_16x16x32_bf16 v[54:57], v[174:177], v[182:185], v[54:57]
	v_mfma_f32_16x16x32_bf16 v[42:45], v[166:169], v[190:193], v[42:45]
	v_mfma_f32_16x16x32_bf16 v[38:41], v[174:177], v[190:193], v[38:41]
	s_setprio 0
	s_setprio 1
	v_mfma_f32_16x16x32_bf16 v[26:29], v[166:169], v[198:201], v[26:29]
	v_mfma_f32_16x16x32_bf16 v[22:25], v[174:177], v[198:201], v[22:25]
	v_mfma_f32_16x16x32_bf16 v[10:13], v[166:169], v[206:209], v[10:13]
	v_mfma_f32_16x16x32_bf16 v[6:9], v[174:177], v[206:209], v[6:9]
	s_setprio 0
	s_barrier
	s_add_i32 s62, 0, 0x18000
	s_add_i32 s63, 0, 0x1c000
	v_add_u32_e32 v158, s62, v148
	v_add_u32_e32 v174, s63, v148
	ds_read_b128 v[144:147], v158
	ds_read_b128 v[150:153], v158 offset:1024
	ds_read_b128 v[154:157], v158 offset:2048
	ds_read_b128 v[158:161], v158 offset:3072
	ds_read_b128 v[162:165], v174
	ds_read_b128 v[166:169], v174 offset:1024
	ds_read_b128 v[170:173], v174 offset:2048
	ds_read_b128 v[174:177], v174 offset:3072
	s_add_u32 s48, s48, 0x40000
	s_addc_u32 s49, s49, 0
	s_mov_b32 m0, s52
	v_lshl_add_u64 v[220:221], s[48:49], 0, v[134:135]
	ds_read_b128 v[178:181], v149 offset:32768
	ds_read_b128 v[182:185], v149 offset:33792
	ds_read_b128 v[186:189], v149 offset:34816
	ds_read_b128 v[190:193], v149 offset:35840
	ds_read_b128 v[194:197], v149 offset:36864
	ds_read_b128 v[198:201], v149 offset:37888
	ds_read_b128 v[202:205], v149 offset:38912
	ds_read_b128 v[206:209], v149 offset:39936
	global_load_lds_dwordx4 v[220:221], off
	v_lshl_add_u64 v[220:221], s[48:49], 0, v[136:137]
	s_mov_b32 m0, s53
	s_nop 0
	global_load_lds_dwordx4 v[220:221], off
	s_waitcnt vmcnt(8)
	s_waitcnt lgkmcnt(0)
	s_barrier
	s_setprio 1
	s_waitcnt lgkmcnt(0)
	v_mfma_f32_16x16x32_bf16 v[130:133], v[144:147], v[178:181], v[130:133]
	v_mfma_f32_16x16x32_bf16 v[126:129], v[154:157], v[178:181], v[126:129]
	v_mfma_f32_16x16x32_bf16 v[114:117], v[144:147], v[186:189], v[114:117]
	v_mfma_f32_16x16x32_bf16 v[110:113], v[154:157], v[186:189], v[110:113]
	s_setprio 0
	s_setprio 1
	v_mfma_f32_16x16x32_bf16 v[98:101], v[144:147], v[194:197], v[98:101]
	v_mfma_f32_16x16x32_bf16 v[94:97], v[154:157], v[194:197], v[94:97]
	v_mfma_f32_16x16x32_bf16 v[82:85], v[144:147], v[202:205], v[82:85]
	v_mfma_f32_16x16x32_bf16 v[78:81], v[154:157], v[202:205], v[78:81]
	s_setprio 0
	s_setprio 1
	v_mfma_f32_16x16x32_bf16 v[130:133], v[150:153], v[182:185], v[130:133]
	v_mfma_f32_16x16x32_bf16 v[126:129], v[158:161], v[182:185], v[126:129]
	v_mfma_f32_16x16x32_bf16 v[114:117], v[150:153], v[190:193], v[114:117]
	v_mfma_f32_16x16x32_bf16 v[110:113], v[158:161], v[190:193], v[110:113]
	s_setprio 0
	s_setprio 1
	v_mfma_f32_16x16x32_bf16 v[98:101], v[150:153], v[198:201], v[98:101]
	v_mfma_f32_16x16x32_bf16 v[94:97], v[158:161], v[198:201], v[94:97]
	v_mfma_f32_16x16x32_bf16 v[82:85], v[150:153], v[206:209], v[82:85]
	v_mfma_f32_16x16x32_bf16 v[78:81], v[158:161], v[206:209], v[78:81]
	s_setprio 0
	s_setprio 1
	v_mfma_f32_16x16x32_bf16 v[122:125], v[162:165], v[178:181], v[122:125]
	v_mfma_f32_16x16x32_bf16 v[118:121], v[170:173], v[178:181], v[118:121]
	v_mfma_f32_16x16x32_bf16 v[106:109], v[162:165], v[186:189], v[106:109]
	v_mfma_f32_16x16x32_bf16 v[102:105], v[170:173], v[186:189], v[102:105]
	s_setprio 0
	s_setprio 1
	v_mfma_f32_16x16x32_bf16 v[90:93], v[162:165], v[194:197], v[90:93]
	v_mfma_f32_16x16x32_bf16 v[86:89], v[170:173], v[194:197], v[86:89]
	v_mfma_f32_16x16x32_bf16 v[74:77], v[162:165], v[202:205], v[74:77]
	v_mfma_f32_16x16x32_bf16 v[70:73], v[170:173], v[202:205], v[70:73]
	s_setprio 0
	s_setprio 1
	v_mfma_f32_16x16x32_bf16 v[122:125], v[166:169], v[182:185], v[122:125]
	v_mfma_f32_16x16x32_bf16 v[118:121], v[174:177], v[182:185], v[118:121]
	v_mfma_f32_16x16x32_bf16 v[106:109], v[166:169], v[190:193], v[106:109]
	v_mfma_f32_16x16x32_bf16 v[102:105], v[174:177], v[190:193], v[102:105]
	s_setprio 0
	s_setprio 1
	v_mfma_f32_16x16x32_bf16 v[90:93], v[166:169], v[198:201], v[90:93]
	v_mfma_f32_16x16x32_bf16 v[86:89], v[174:177], v[198:201], v[86:89]
	v_mfma_f32_16x16x32_bf16 v[74:77], v[166:169], v[206:209], v[74:77]
	v_mfma_f32_16x16x32_bf16 v[70:73], v[174:177], v[206:209], v[70:73]
	s_setprio 0
	s_barrier
	s_add_i32 s48, s62, s27
	v_lshl_add_u64 v[210:211], v[210:211], 0, s[66:67]
	s_mov_b32 m0, s48
	ds_read_b128 v[178:181], v149 offset:49152
	ds_read_b128 v[182:185], v149 offset:50176
	ds_read_b128 v[186:189], v149 offset:51200
	ds_read_b128 v[190:193], v149 offset:52224
	ds_read_b128 v[194:197], v149 offset:53248
	ds_read_b128 v[198:201], v149 offset:54272
	ds_read_b128 v[202:205], v149 offset:55296
	ds_read_b128 v[206:209], v149 offset:56320
	global_load_lds_dwordx4 v[210:211], off
	s_add_i32 m0, s48, 0x2000
	s_add_u32 s46, s46, 0x40080
	v_lshl_add_u64 v[210:211], v[212:213], 0, s[66:67]
	s_addc_u32 s47, s47, 0
	s_add_i32 s48, s63, s27
	global_load_lds_dwordx4 v[210:211], off
	v_lshl_add_u64 v[210:211], s[46:47], 0, v[0:1]
	s_mov_b32 m0, s48
	s_nop 0
	global_load_lds_dwordx4 v[210:211], off
	v_lshl_add_u64 v[210:211], s[46:47], 0, v[138:139]
	s_add_i32 m0, s48, 0x2000
	s_nop 0
	global_load_lds_dwordx4 v[210:211], off
	v_lshl_add_u64 v[210:211], v[216:217], 0, s[66:67]
	s_mov_b32 m0, s56
	s_nop 0
	global_load_lds_dwordx4 v[210:211], off
	v_lshl_add_u64 v[210:211], v[218:219], 0, s[66:67]
	s_mov_b32 m0, s57
	s_nop 0
	global_load_lds_dwordx4 v[210:211], off
	s_waitcnt vmcnt(8)
	s_waitcnt lgkmcnt(0)
	s_barrier
	s_setprio 1
	s_waitcnt lgkmcnt(0)
	v_mfma_f32_16x16x32_bf16 v[66:69], v[144:147], v[178:181], v[66:69]
	v_mfma_f32_16x16x32_bf16 v[62:65], v[154:157], v[178:181], v[62:65]
	v_mfma_f32_16x16x32_bf16 v[50:53], v[144:147], v[186:189], v[50:53]
	v_mfma_f32_16x16x32_bf16 v[46:49], v[154:157], v[186:189], v[46:49]
	s_setprio 0
	s_setprio 1
	v_mfma_f32_16x16x32_bf16 v[34:37], v[144:147], v[194:197], v[34:37]
	v_mfma_f32_16x16x32_bf16 v[30:33], v[154:157], v[194:197], v[30:33]
	v_mfma_f32_16x16x32_bf16 v[18:21], v[144:147], v[202:205], v[18:21]
	v_mfma_f32_16x16x32_bf16 v[14:17], v[154:157], v[202:205], v[14:17]
	s_setprio 0
	s_setprio 1
	v_mfma_f32_16x16x32_bf16 v[66:69], v[150:153], v[182:185], v[66:69]
	v_mfma_f32_16x16x32_bf16 v[62:65], v[158:161], v[182:185], v[62:65]
	v_mfma_f32_16x16x32_bf16 v[50:53], v[150:153], v[190:193], v[50:53]
	v_mfma_f32_16x16x32_bf16 v[46:49], v[158:161], v[190:193], v[46:49]
	s_setprio 0
	s_setprio 1
	v_mfma_f32_16x16x32_bf16 v[34:37], v[150:153], v[198:201], v[34:37]
	v_mfma_f32_16x16x32_bf16 v[30:33], v[158:161], v[198:201], v[30:33]
	v_mfma_f32_16x16x32_bf16 v[18:21], v[150:153], v[206:209], v[18:21]
	v_mfma_f32_16x16x32_bf16 v[14:17], v[158:161], v[206:209], v[14:17]
	s_setprio 0
	s_setprio 1
	v_mfma_f32_16x16x32_bf16 v[58:61], v[162:165], v[178:181], v[58:61]
	v_mfma_f32_16x16x32_bf16 v[54:57], v[170:173], v[178:181], v[54:57]
	v_mfma_f32_16x16x32_bf16 v[42:45], v[162:165], v[186:189], v[42:45]
	v_mfma_f32_16x16x32_bf16 v[38:41], v[170:173], v[186:189], v[38:41]
	s_setprio 0
	s_setprio 1
	v_mfma_f32_16x16x32_bf16 v[26:29], v[162:165], v[194:197], v[26:29]
	v_mfma_f32_16x16x32_bf16 v[22:25], v[170:173], v[194:197], v[22:25]
	v_mfma_f32_16x16x32_bf16 v[10:13], v[162:165], v[202:205], v[10:13]
	v_mfma_f32_16x16x32_bf16 v[6:9], v[170:173], v[202:205], v[6:9]
	s_setprio 0
	s_setprio 1
	v_mfma_f32_16x16x32_bf16 v[58:61], v[166:169], v[182:185], v[58:61]
	v_mfma_f32_16x16x32_bf16 v[54:57], v[174:177], v[182:185], v[54:57]
	v_mfma_f32_16x16x32_bf16 v[42:45], v[166:169], v[190:193], v[42:45]
	v_mfma_f32_16x16x32_bf16 v[38:41], v[174:177], v[190:193], v[38:41]
	s_setprio 0
	s_setprio 1
	v_mfma_f32_16x16x32_bf16 v[26:29], v[166:169], v[198:201], v[26:29]
	v_mfma_f32_16x16x32_bf16 v[22:25], v[174:177], v[198:201], v[22:25]
	v_mfma_f32_16x16x32_bf16 v[10:13], v[166:169], v[206:209], v[10:13]
	v_mfma_f32_16x16x32_bf16 v[6:9], v[174:177], v[206:209], v[6:9]
	s_setprio 0
	s_barrier
	s_add_i32 s61, s61, 2
	s_add_u32 s44, s44, 0x100
	s_addc_u32 s45, s45, 0
	s_add_u32 s59, s59, 0x100
	s_addc_u32 s60, s60, 0
	s_cmp_gt_u32 s61, 13
	s_cbranch_scc0 .LBB0_290
	s_and_b64 vcc, exec, s[30:31]
	s_cbranch_vccz .LBB0_293
	s_barrier

.Lrw_done_ip8_0:
	s_waitcnt lgkmcnt(0)
	s_barrier
	s_setprio 1
	s_waitcnt lgkmcnt(0)
	v_mfma_scale_f32_16x16x128_f8f6f4 v[158:161], v[18:25], v[172:179], 0, v234, v235 op_sel_hi:[0,0,0]
	v_mfma_scale_f32_16x16x128_f8f6f4 v[154:157], v[26:33], v[172:179], 0, v234, v235 op_sel_hi:[0,0,0]
	s_setprio 0
	s_setprio 1
	v_mfma_scale_f32_16x16x128_f8f6f4 v[150:153], v[18:25], v[198:205], 0, v234, v235 op_sel_hi:[0,0,0]
	v_mfma_scale_f32_16x16x128_f8f6f4 v[146:149], v[26:33], v[198:205], 0, v234, v235 op_sel_hi:[0,0,0]
	s_setprio 0
	s_setprio 1
	v_mfma_scale_f32_16x16x128_f8f6f4 v[142:145], v[18:25], v[206:213], 0, v234, v235 op_sel_hi:[0,0,0]
	v_mfma_scale_f32_16x16x128_f8f6f4 v[138:141], v[26:33], v[206:213], 0, v234, v235 op_sel_hi:[0,0,0]
	s_setprio 0
	s_setprio 1
	v_mfma_scale_f32_16x16x128_f8f6f4 v[134:137], v[18:25], v[216:223], 0, v234, v235 op_sel_hi:[0,0,0]
	v_mfma_scale_f32_16x16x128_f8f6f4 v[130:133], v[26:33], v[216:223], 0, v234, v235 op_sel_hi:[0,0,0]
	s_setprio 0
	s_setprio 1
	v_mfma_scale_f32_16x16x128_f8f6f4 v[126:129], v[2:9], v[172:179], 0, v234, v235 op_sel_hi:[0,0,0]
	v_mfma_scale_f32_16x16x128_f8f6f4 v[122:125], v[10:17], v[172:179], 0, v234, v235 op_sel_hi:[0,0,0]
	s_setprio 0
	s_setprio 1
	v_mfma_scale_f32_16x16x128_f8f6f4 v[118:121], v[2:9], v[198:205], 0, v234, v235 op_sel_hi:[0,0,0]
	v_mfma_scale_f32_16x16x128_f8f6f4 v[114:117], v[10:17], v[198:205], 0, v234, v235 op_sel_hi:[0,0,0]
	s_setprio 0
	s_setprio 1
	v_mfma_scale_f32_16x16x128_f8f6f4 v[110:113], v[2:9], v[206:213], 0, v234, v235 op_sel_hi:[0,0,0]
	v_mfma_scale_f32_16x16x128_f8f6f4 v[106:109], v[10:17], v[206:213], 0, v234, v235 op_sel_hi:[0,0,0]
	s_setprio 0
	s_setprio 1
	v_mfma_scale_f32_16x16x128_f8f6f4 v[102:105], v[2:9], v[216:223], 0, v234, v235 op_sel_hi:[0,0,0]
	v_mfma_scale_f32_16x16x128_f8f6f4 v[98:101], v[10:17], v[216:223], 0, v234, v235 op_sel_hi:[0,0,0]
	s_setprio 0
	s_barrier
	v_lshl_add_u64 v[172:173], s[44:45], 0, v[0:1]
	s_mov_b64 s[74:75], 0x100
	s_mov_b32 m0, s58
	v_lshl_add_u64 v[174:175], v[172:173], 0, s[74:75]
	ds_read_b128 v[198:201], v196 offset:16384
	ds_read_b128 v[202:205], v196 offset:17408
	ds_read_b128 v[206:209], v196 offset:18432
	ds_read_b128 v[210:213], v196 offset:19456
	ds_read_b128 v[216:219], v196 offset:20480
	ds_read_b128 v[220:223], v196 offset:21504
	ds_read_b128 v[224:227], v196 offset:22528
	ds_read_b128 v[228:231], v196 offset:23552
	global_load_lds_dwordx4 v[174:175], off
	v_lshl_add_u64 v[174:175], s[44:45], 0, v[166:167]
	s_add_u32 s48, s44, 0x20100
	v_lshl_add_u64 v[176:177], v[174:175], 0, s[74:75]
	s_mov_b32 m0, s59
	s_addc_u32 s49, s45, 0
	global_load_lds_dwordx4 v[176:177], off
	v_lshl_add_u64 v[176:177], s[48:49], 0, v[0:1]
	s_mov_b32 m0, s60
	s_nop 0
	global_load_lds_dwordx4 v[176:177], off
	v_lshl_add_u64 v[176:177], s[48:49], 0, v[166:167]
	s_mov_b32 m0, s61
	s_nop 0
	global_load_lds_dwordx4 v[176:177], off
	v_lshl_add_u64 v[176:177], s[46:47], 0, v[162:163]
	v_lshl_add_u64 v[178:179], v[176:177], 0, s[74:75]
	s_mov_b32 m0, s57
	s_nop 0
	global_load_lds_dwordx4 v[178:179], off
	v_lshl_add_u64 v[178:179], s[46:47], 0, v[164:165]
	v_lshl_add_u64 v[232:233], v[178:179], 0, s[74:75]
	s_mov_b32 m0, s62
	s_nop 0
	global_load_lds_dwordx4 v[232:233], off
	s_cmp_eq_u32 s50, 1
	s_cbranch_scc1 .Lrw_first_ip8_1
	s_waitcnt vmcnt(24)
	s_branch .Lrw_done_ip8_1

.Lrw_done_ip8_1:
	s_waitcnt lgkmcnt(0)
	s_barrier
	s_setprio 1
	s_waitcnt lgkmcnt(0)
	v_mfma_scale_f32_16x16x128_f8f6f4 v[94:97], v[18:25], v[198:205], 0, v234, v235 op_sel_hi:[0,0,0]
	v_mfma_scale_f32_16x16x128_f8f6f4 v[90:93], v[26:33], v[198:205], 0, v234, v235 op_sel_hi:[0,0,0]
	s_setprio 0
	s_setprio 1
	v_mfma_scale_f32_16x16x128_f8f6f4 v[86:89], v[18:25], v[206:213], 0, v234, v235 op_sel_hi:[0,0,0]
	v_mfma_scale_f32_16x16x128_f8f6f4 v[82:85], v[26:33], v[206:213], 0, v234, v235 op_sel_hi:[0,0,0]
	s_setprio 0
	s_setprio 1
	v_mfma_scale_f32_16x16x128_f8f6f4 v[78:81], v[18:25], v[216:223], 0, v234, v235 op_sel_hi:[0,0,0]
	v_mfma_scale_f32_16x16x128_f8f6f4 v[74:77], v[26:33], v[216:223], 0, v234, v235 op_sel_hi:[0,0,0]
	s_setprio 0
	s_setprio 1
	v_mfma_scale_f32_16x16x128_f8f6f4 v[70:73], v[18:25], v[224:231], 0, v234, v235 op_sel_hi:[0,0,0]
	v_mfma_scale_f32_16x16x128_f8f6f4 v[66:69], v[26:33], v[224:231], 0, v234, v235 op_sel_hi:[0,0,0]
	s_setprio 0
	s_setprio 1
	v_mfma_scale_f32_16x16x128_f8f6f4 v[62:65], v[2:9], v[198:205], 0, v234, v235 op_sel_hi:[0,0,0]
	v_mfma_scale_f32_16x16x128_f8f6f4 v[58:61], v[10:17], v[198:205], 0, v234, v235 op_sel_hi:[0,0,0]
	s_setprio 0
	s_setprio 1
	v_mfma_scale_f32_16x16x128_f8f6f4 v[54:57], v[2:9], v[206:213], 0, v234, v235 op_sel_hi:[0,0,0]
	v_mfma_scale_f32_16x16x128_f8f6f4 v[50:53], v[10:17], v[206:213], 0, v234, v235 op_sel_hi:[0,0,0]
	s_setprio 0
	s_setprio 1
	v_mfma_scale_f32_16x16x128_f8f6f4 v[46:49], v[2:9], v[216:223], 0, v234, v235 op_sel_hi:[0,0,0]
	v_mfma_scale_f32_16x16x128_f8f6f4 v[42:45], v[10:17], v[216:223], 0, v234, v235 op_sel_hi:[0,0,0]
	s_setprio 0
	s_setprio 1
	v_mfma_scale_f32_16x16x128_f8f6f4 v[38:41], v[2:9], v[224:231], 0, v234, v235 op_sel_hi:[0,0,0]
	v_mfma_scale_f32_16x16x128_f8f6f4 v[34:37], v[10:17], v[224:231], 0, v234, v235 op_sel_hi:[0,0,0]
	s_setprio 0
	s_barrier
	ds_read_b128 v[18:21], v188
	ds_read_b128 v[22:25], v189
	ds_read_b128 v[26:29], v190
	ds_read_b128 v[30:33], v191
	ds_read_b128 v[2:5], v192
	ds_read_b128 v[6:9], v193
	ds_read_b128 v[10:13], v194
	ds_read_b128 v[14:17], v195
	s_add_u32 s48, s46, 0x20100
	s_addc_u32 s49, s47, 0
	s_mov_b32 m0, s63
	v_lshl_add_u64 v[232:233], s[48:49], 0, v[162:163]
	ds_read_b128 v[198:201], v196 offset:32768
	ds_read_b128 v[202:205], v196 offset:33792
	ds_read_b128 v[206:209], v196 offset:34816
	ds_read_b128 v[210:213], v196 offset:35840
	ds_read_b128 v[216:219], v196 offset:36864
	ds_read_b128 v[220:223], v196 offset:37888
	ds_read_b128 v[224:227], v196 offset:38912
	ds_read_b128 v[228:231], v196 offset:39936
	global_load_lds_dwordx4 v[232:233], off
	v_lshl_add_u64 v[232:233], s[48:49], 0, v[164:165]
	s_mov_b32 m0, s64
	s_nop 0
	global_load_lds_dwordx4 v[232:233], off
	s_waitcnt vmcnt(8)
	s_waitcnt lgkmcnt(0)
	s_barrier
	s_setprio 1
	s_waitcnt lgkmcnt(0)
	v_mfma_scale_f32_16x16x128_f8f6f4 v[158:161], v[18:25], v[198:205], v[158:161], v234, v235 op_sel_hi:[0,0,0]
	v_mfma_scale_f32_16x16x128_f8f6f4 v[154:157], v[26:33], v[198:205], v[154:157], v234, v235 op_sel_hi:[0,0,0]
	s_setprio 0
	s_setprio 1
	v_mfma_scale_f32_16x16x128_f8f6f4 v[150:153], v[18:25], v[206:213], v[150:153], v234, v235 op_sel_hi:[0,0,0]
	v_mfma_scale_f32_16x16x128_f8f6f4 v[146:149], v[26:33], v[206:213], v[146:149], v234, v235 op_sel_hi:[0,0,0]
	s_setprio 0
	s_setprio 1
	v_mfma_scale_f32_16x16x128_f8f6f4 v[142:145], v[18:25], v[216:223], v[142:145], v234, v235 op_sel_hi:[0,0,0]
	v_mfma_scale_f32_16x16x128_f8f6f4 v[138:141], v[26:33], v[216:223], v[138:141], v234, v235 op_sel_hi:[0,0,0]
	s_setprio 0
	s_setprio 1
	v_mfma_scale_f32_16x16x128_f8f6f4 v[134:137], v[18:25], v[224:231], v[134:137], v234, v235 op_sel_hi:[0,0,0]
	v_mfma_scale_f32_16x16x128_f8f6f4 v[130:133], v[26:33], v[224:231], v[130:133], v234, v235 op_sel_hi:[0,0,0]
	s_setprio 0
	s_setprio 1
	v_mfma_scale_f32_16x16x128_f8f6f4 v[126:129], v[2:9], v[198:205], v[126:129], v234, v235 op_sel_hi:[0,0,0]
	v_mfma_scale_f32_16x16x128_f8f6f4 v[122:125], v[10:17], v[198:205], v[122:125], v234, v235 op_sel_hi:[0,0,0]
	s_setprio 0
	s_setprio 1
	v_mfma_scale_f32_16x16x128_f8f6f4 v[118:121], v[2:9], v[206:213], v[118:121], v234, v235 op_sel_hi:[0,0,0]
	v_mfma_scale_f32_16x16x128_f8f6f4 v[114:117], v[10:17], v[206:213], v[114:117], v234, v235 op_sel_hi:[0,0,0]
	s_setprio 0
	s_setprio 1
	v_mfma_scale_f32_16x16x128_f8f6f4 v[110:113], v[2:9], v[216:223], v[110:113], v234, v235 op_sel_hi:[0,0,0]
	v_mfma_scale_f32_16x16x128_f8f6f4 v[106:109], v[10:17], v[216:223], v[106:109], v234, v235 op_sel_hi:[0,0,0]
	s_setprio 0
	s_setprio 1
	v_mfma_scale_f32_16x16x128_f8f6f4 v[102:105], v[2:9], v[224:231], v[102:105], v234, v235 op_sel_hi:[0,0,0]
	v_mfma_scale_f32_16x16x128_f8f6f4 v[98:101], v[10:17], v[224:231], v[98:101], v234, v235 op_sel_hi:[0,0,0]
	s_setprio 0
	s_barrier
	s_mov_b64 s[74:75], 0x180
	s_mov_b32 m0, s7
	v_lshl_add_u64 v[172:173], v[172:173], 0, s[74:75]
	s_add_u32 s48, s44, 0x20180
	ds_read_b128 v[198:201], v196 offset:49152
	ds_read_b128 v[202:205], v196 offset:50176
	ds_read_b128 v[206:209], v196 offset:51200
	ds_read_b128 v[210:213], v196 offset:52224
	ds_read_b128 v[216:219], v196 offset:53248
	ds_read_b128 v[220:223], v196 offset:54272
	ds_read_b128 v[224:227], v196 offset:55296
	ds_read_b128 v[228:231], v196 offset:56320
	global_load_lds_dwordx4 v[172:173], off
	v_lshl_add_u64 v[172:173], v[174:175], 0, s[74:75]
	s_mov_b32 m0, s65
	s_addc_u32 s49, s45, 0
	global_load_lds_dwordx4 v[172:173], off
	v_lshl_add_u64 v[172:173], s[48:49], 0, v[0:1]
	s_mov_b32 m0, s13
	s_nop 0
	global_load_lds_dwordx4 v[172:173], off
	v_lshl_add_u64 v[172:173], s[48:49], 0, v[166:167]
	s_mov_b32 m0, s51
	s_nop 0
	global_load_lds_dwordx4 v[172:173], off
	v_lshl_add_u64 v[172:173], v[176:177], 0, s[74:75]
	s_mov_b32 m0, s68
	s_nop 0
	global_load_lds_dwordx4 v[172:173], off
	v_lshl_add_u64 v[172:173], v[178:179], 0, s[74:75]
	s_mov_b32 m0, s52
	s_nop 0
	global_load_lds_dwordx4 v[172:173], off
	s_waitcnt vmcnt(8)
	s_waitcnt lgkmcnt(0)
	s_barrier
	s_setprio 1
	s_waitcnt lgkmcnt(0)
	v_mfma_scale_f32_16x16x128_f8f6f4 v[94:97], v[18:25], v[198:205], v[94:97], v234, v235 op_sel_hi:[0,0,0]
	v_mfma_scale_f32_16x16x128_f8f6f4 v[90:93], v[26:33], v[198:205], v[90:93], v234, v235 op_sel_hi:[0,0,0]
	s_setprio 0
	s_setprio 1
	v_mfma_scale_f32_16x16x128_f8f6f4 v[86:89], v[18:25], v[206:213], v[86:89], v234, v235 op_sel_hi:[0,0,0]
	v_mfma_scale_f32_16x16x128_f8f6f4 v[82:85], v[26:33], v[206:213], v[82:85], v234, v235 op_sel_hi:[0,0,0]
	s_setprio 0
	s_setprio 1
	v_mfma_scale_f32_16x16x128_f8f6f4 v[78:81], v[18:25], v[216:223], v[78:81], v234, v235 op_sel_hi:[0,0,0]
	v_mfma_scale_f32_16x16x128_f8f6f4 v[74:77], v[26:33], v[216:223], v[74:77], v234, v235 op_sel_hi:[0,0,0]
	s_setprio 0
	s_setprio 1
	v_mfma_scale_f32_16x16x128_f8f6f4 v[70:73], v[18:25], v[224:231], v[70:73], v234, v235 op_sel_hi:[0,0,0]
	v_mfma_scale_f32_16x16x128_f8f6f4 v[66:69], v[26:33], v[224:231], v[66:69], v234, v235 op_sel_hi:[0,0,0]
	s_setprio 0
	s_setprio 1
	v_mfma_scale_f32_16x16x128_f8f6f4 v[62:65], v[2:9], v[198:205], v[62:65], v234, v235 op_sel_hi:[0,0,0]
	v_mfma_scale_f32_16x16x128_f8f6f4 v[58:61], v[10:17], v[198:205], v[58:61], v234, v235 op_sel_hi:[0,0,0]
	s_setprio 0
	s_setprio 1
	v_mfma_scale_f32_16x16x128_f8f6f4 v[54:57], v[2:9], v[206:213], v[54:57], v234, v235 op_sel_hi:[0,0,0]
	v_mfma_scale_f32_16x16x128_f8f6f4 v[50:53], v[10:17], v[206:213], v[50:53], v234, v235 op_sel_hi:[0,0,0]
	s_setprio 0
	s_setprio 1
	v_mfma_scale_f32_16x16x128_f8f6f4 v[46:49], v[2:9], v[216:223], v[46:49], v234, v235 op_sel_hi:[0,0,0]
	v_mfma_scale_f32_16x16x128_f8f6f4 v[42:45], v[10:17], v[216:223], v[42:45], v234, v235 op_sel_hi:[0,0,0]
	s_setprio 0
	s_setprio 1
	v_mfma_scale_f32_16x16x128_f8f6f4 v[38:41], v[2:9], v[224:231], v[38:41], v234, v235 op_sel_hi:[0,0,0]
	v_mfma_scale_f32_16x16x128_f8f6f4 v[34:37], v[10:17], v[224:231], v[34:37], v234, v235 op_sel_hi:[0,0,0]
	s_setprio 0
	s_barrier
	s_add_u32 s46, s46, 0x20180
	s_addc_u32 s47, s47, 0
	s_add_u32 s37, s44, 0x200
	s_addc_u32 s74, s45, 0
	s_mov_b32 s75, 0
.LBB0_388:
	ds_read_b128 v[2:5], v180
	ds_read_b128 v[6:9], v181
	ds_read_b128 v[10:13], v182
	ds_read_b128 v[14:17], v183
	ds_read_b128 v[26:29], v184
	ds_read_b128 v[30:33], v185
	ds_read_b128 v[172:175], v186
	ds_read_b128 v[176:179], v187
	s_add_u32 s44, s46, 0xfffe0080
	s_addc_u32 s45, s47, -1
	s_cmp_eq_u32 s75, 4
	s_cselect_b32 s49, s1, s45
	s_cselect_b32 s48, s5, s44
	s_cselect_b32 s45, s23, s74
	s_cselect_b32 s44, s26, s37
	s_mov_b32 m0, s27
	v_lshl_add_u64 v[224:225], s[46:47], 0, v[168:169]
	ds_read_b128 v[18:21], v196
	ds_read_b128 v[22:25], v196 offset:1024
	ds_read_b128 v[198:201], v196 offset:2048
	ds_read_b128 v[202:205], v196 offset:3072
	ds_read_b128 v[206:209], v196 offset:4096
	ds_read_b128 v[210:213], v196 offset:5120
	ds_read_b128 v[216:219], v196 offset:6144
	ds_read_b128 v[220:223], v196 offset:7168
	global_load_lds_dwordx4 v[224:225], off
	v_lshl_add_u64 v[224:225], s[46:47], 0, v[170:171]
	s_mov_b32 m0, s35
	s_nop 0
	global_load_lds_dwordx4 v[224:225], off
	s_waitcnt vmcnt(8)
	s_waitcnt lgkmcnt(0)
	s_barrier
	s_setprio 1
	s_waitcnt lgkmcnt(0)
	v_mfma_scale_f32_16x16x128_f8f6f4 v[158:161], v[2:9], v[18:25], v[158:161], v234, v235 op_sel_hi:[0,0,0]
	v_mfma_scale_f32_16x16x128_f8f6f4 v[154:157], v[10:17], v[18:25], v[154:157], v234, v235 op_sel_hi:[0,0,0]
	s_setprio 0
	s_setprio 1
	v_mfma_scale_f32_16x16x128_f8f6f4 v[150:153], v[2:9], v[198:205], v[150:153], v234, v235 op_sel_hi:[0,0,0]
	v_mfma_scale_f32_16x16x128_f8f6f4 v[146:149], v[10:17], v[198:205], v[146:149], v234, v235 op_sel_hi:[0,0,0]
	s_setprio 0
	s_setprio 1
	v_mfma_scale_f32_16x16x128_f8f6f4 v[142:145], v[2:9], v[206:213], v[142:145], v234, v235 op_sel_hi:[0,0,0]
	v_mfma_scale_f32_16x16x128_f8f6f4 v[138:141], v[10:17], v[206:213], v[138:141], v234, v235 op_sel_hi:[0,0,0]
	s_setprio 0
	s_setprio 1
	v_mfma_scale_f32_16x16x128_f8f6f4 v[134:137], v[2:9], v[216:223], v[134:137], v234, v235 op_sel_hi:[0,0,0]
	v_mfma_scale_f32_16x16x128_f8f6f4 v[130:133], v[10:17], v[216:223], v[130:133], v234, v235 op_sel_hi:[0,0,0]
	s_setprio 0
	s_setprio 1
	v_mfma_scale_f32_16x16x128_f8f6f4 v[126:129], v[26:33], v[18:25], v[126:129], v234, v235 op_sel_hi:[0,0,0]
	v_mfma_scale_f32_16x16x128_f8f6f4 v[122:125], v[172:179], v[18:25], v[122:125], v234, v235 op_sel_hi:[0,0,0]
	s_setprio 0
	s_setprio 1
	v_mfma_scale_f32_16x16x128_f8f6f4 v[118:121], v[26:33], v[198:205], v[118:121], v234, v235 op_sel_hi:[0,0,0]
	v_mfma_scale_f32_16x16x128_f8f6f4 v[114:117], v[172:179], v[198:205], v[114:117], v234, v235 op_sel_hi:[0,0,0]
	s_setprio 0
	s_setprio 1
	v_mfma_scale_f32_16x16x128_f8f6f4 v[110:113], v[26:33], v[206:213], v[110:113], v234, v235 op_sel_hi:[0,0,0]
	v_mfma_scale_f32_16x16x128_f8f6f4 v[106:109], v[172:179], v[206:213], v[106:109], v234, v235 op_sel_hi:[0,0,0]
	s_setprio 0
	s_setprio 1
	v_mfma_scale_f32_16x16x128_f8f6f4 v[102:105], v[26:33], v[216:223], v[102:105], v234, v235 op_sel_hi:[0,0,0]
	v_mfma_scale_f32_16x16x128_f8f6f4 v[98:101], v[172:179], v[216:223], v[98:101], v234, v235 op_sel_hi:[0,0,0]
	s_setprio 0
	s_barrier
	s_mov_b32 m0, s58
	v_lshl_add_u64 v[18:19], s[44:45], 0, v[0:1]
	s_add_u32 vcc_lo, s44, 0x20000
	ds_read_b128 v[198:201], v196 offset:16384
	ds_read_b128 v[202:205], v196 offset:17408
	ds_read_b128 v[206:209], v196 offset:18432
	ds_read_b128 v[210:213], v196 offset:19456
	ds_read_b128 v[216:219], v196 offset:20480
	ds_read_b128 v[220:223], v196 offset:21504
	ds_read_b128 v[224:227], v196 offset:22528
	ds_read_b128 v[228:231], v196 offset:23552
	global_load_lds_dwordx4 v[18:19], off
	v_lshl_add_u64 v[20:21], s[44:45], 0, v[166:167]
	s_mov_b32 m0, s59
	s_addc_u32 vcc_hi, s45, 0
	global_load_lds_dwordx4 v[20:21], off
	v_lshl_add_u64 v[22:23], vcc, 0, v[0:1]
	s_mov_b32 m0, s60
	v_lshl_add_u64 v[24:25], s[48:49], 0, v[164:165]
	global_load_lds_dwordx4 v[22:23], off
	v_lshl_add_u64 v[22:23], vcc, 0, v[166:167]
	s_mov_b32 m0, s61
	s_nop 0
	global_load_lds_dwordx4 v[22:23], off
	v_lshl_add_u64 v[22:23], s[48:49], 0, v[162:163]
	s_mov_b32 m0, s57
	s_nop 0
	global_load_lds_dwordx4 v[22:23], off
	s_mov_b32 m0, s62
	s_nop 0
	global_load_lds_dwordx4 v[24:25], off
	s_waitcnt vmcnt(8)
	s_waitcnt lgkmcnt(0)
	s_barrier
	s_setprio 1
	s_waitcnt lgkmcnt(0)
	v_mfma_scale_f32_16x16x128_f8f6f4 v[94:97], v[2:9], v[198:205], v[94:97], v234, v235 op_sel_hi:[0,0,0]
	v_mfma_scale_f32_16x16x128_f8f6f4 v[90:93], v[10:17], v[198:205], v[90:93], v234, v235 op_sel_hi:[0,0,0]
	s_setprio 0
	s_setprio 1
	v_mfma_scale_f32_16x16x128_f8f6f4 v[86:89], v[2:9], v[206:213], v[86:89], v234, v235 op_sel_hi:[0,0,0]
	v_mfma_scale_f32_16x16x128_f8f6f4 v[82:85], v[10:17], v[206:213], v[82:85], v234, v235 op_sel_hi:[0,0,0]
	s_setprio 0
	s_setprio 1
	v_mfma_scale_f32_16x16x128_f8f6f4 v[78:81], v[2:9], v[216:223], v[78:81], v234, v235 op_sel_hi:[0,0,0]
	v_mfma_scale_f32_16x16x128_f8f6f4 v[74:77], v[10:17], v[216:223], v[74:77], v234, v235 op_sel_hi:[0,0,0]
	s_setprio 0
	s_setprio 1
	v_mfma_scale_f32_16x16x128_f8f6f4 v[70:73], v[2:9], v[224:231], v[70:73], v234, v235 op_sel_hi:[0,0,0]
	v_mfma_scale_f32_16x16x128_f8f6f4 v[66:69], v[10:17], v[224:231], v[66:69], v234, v235 op_sel_hi:[0,0,0]
	s_setprio 0
	s_setprio 1
	v_mfma_scale_f32_16x16x128_f8f6f4 v[62:65], v[26:33], v[198:205], v[62:65], v234, v235 op_sel_hi:[0,0,0]
	v_mfma_scale_f32_16x16x128_f8f6f4 v[58:61], v[172:179], v[198:205], v[58:61], v234, v235 op_sel_hi:[0,0,0]
	s_setprio 0
	s_setprio 1
	v_mfma_scale_f32_16x16x128_f8f6f4 v[54:57], v[26:33], v[206:213], v[54:57], v234, v235 op_sel_hi:[0,0,0]
	v_mfma_scale_f32_16x16x128_f8f6f4 v[50:53], v[172:179], v[206:213], v[50:53], v234, v235 op_sel_hi:[0,0,0]
	s_setprio 0
	s_setprio 1
	v_mfma_scale_f32_16x16x128_f8f6f4 v[46:49], v[26:33], v[216:223], v[46:49], v234, v235 op_sel_hi:[0,0,0]
	v_mfma_scale_f32_16x16x128_f8f6f4 v[42:45], v[172:179], v[216:223], v[42:45], v234, v235 op_sel_hi:[0,0,0]
	s_setprio 0
	s_setprio 1
	v_mfma_scale_f32_16x16x128_f8f6f4 v[38:41], v[26:33], v[224:231], v[38:41], v234, v235 op_sel_hi:[0,0,0]
	v_mfma_scale_f32_16x16x128_f8f6f4 v[34:37], v[172:179], v[224:231], v[34:37], v234, v235 op_sel_hi:[0,0,0]
	s_setprio 0
	s_barrier
	ds_read_b128 v[10:13], v188
	ds_read_b128 v[14:17], v189
	ds_read_b128 v[26:29], v190
	ds_read_b128 v[30:33], v191
	ds_read_b128 v[2:5], v192
	ds_read_b128 v[6:9], v193
	ds_read_b128 v[172:175], v194
	ds_read_b128 v[176:179], v195
	s_add_u32 s48, s48, 0x20000
	s_addc_u32 s49, s49, 0
	s_mov_b32 m0, s63
	v_lshl_add_u64 v[232:233], s[48:49], 0, v[162:163]
	ds_read_b128 v[198:201], v196 offset:32768
	ds_read_b128 v[202:205], v196 offset:33792
	ds_read_b128 v[206:209], v196 offset:34816
	ds_read_b128 v[210:213], v196 offset:35840
	ds_read_b128 v[216:219], v196 offset:36864
	ds_read_b128 v[220:223], v196 offset:37888
	ds_read_b128 v[224:227], v196 offset:38912
	ds_read_b128 v[228:231], v196 offset:39936
	global_load_lds_dwordx4 v[232:233], off
	v_lshl_add_u64 v[232:233], s[48:49], 0, v[164:165]
	s_mov_b32 m0, s64
	s_nop 0
	global_load_lds_dwordx4 v[232:233], off
	s_waitcnt vmcnt(8)
	s_waitcnt lgkmcnt(0)
	s_barrier
	s_setprio 1
	s_waitcnt lgkmcnt(0)
	v_mfma_scale_f32_16x16x128_f8f6f4 v[158:161], v[10:17], v[198:205], v[158:161], v234, v235 op_sel_hi:[0,0,0]
	v_mfma_scale_f32_16x16x128_f8f6f4 v[154:157], v[26:33], v[198:205], v[154:157], v234, v235 op_sel_hi:[0,0,0]
	s_setprio 0
	s_setprio 1
	v_mfma_scale_f32_16x16x128_f8f6f4 v[150:153], v[10:17], v[206:213], v[150:153], v234, v235 op_sel_hi:[0,0,0]
	v_mfma_scale_f32_16x16x128_f8f6f4 v[146:149], v[26:33], v[206:213], v[146:149], v234, v235 op_sel_hi:[0,0,0]
	s_setprio 0
	s_setprio 1
	v_mfma_scale_f32_16x16x128_f8f6f4 v[142:145], v[10:17], v[216:223], v[142:145], v234, v235 op_sel_hi:[0,0,0]
	v_mfma_scale_f32_16x16x128_f8f6f4 v[138:141], v[26:33], v[216:223], v[138:141], v234, v235 op_sel_hi:[0,0,0]
	s_setprio 0
	s_setprio 1
	v_mfma_scale_f32_16x16x128_f8f6f4 v[134:137], v[10:17], v[224:231], v[134:137], v234, v235 op_sel_hi:[0,0,0]
	v_mfma_scale_f32_16x16x128_f8f6f4 v[130:133], v[26:33], v[224:231], v[130:133], v234, v235 op_sel_hi:[0,0,0]
	s_setprio 0
	s_setprio 1
	v_mfma_scale_f32_16x16x128_f8f6f4 v[126:129], v[2:9], v[198:205], v[126:129], v234, v235 op_sel_hi:[0,0,0]
	v_mfma_scale_f32_16x16x128_f8f6f4 v[122:125], v[172:179], v[198:205], v[122:125], v234, v235 op_sel_hi:[0,0,0]
	s_setprio 0
	s_setprio 1
	v_mfma_scale_f32_16x16x128_f8f6f4 v[118:121], v[2:9], v[206:213], v[118:121], v234, v235 op_sel_hi:[0,0,0]
	v_mfma_scale_f32_16x16x128_f8f6f4 v[114:117], v[172:179], v[206:213], v[114:117], v234, v235 op_sel_hi:[0,0,0]
	s_setprio 0
	s_setprio 1
	v_mfma_scale_f32_16x16x128_f8f6f4 v[110:113], v[2:9], v[216:223], v[110:113], v234, v235 op_sel_hi:[0,0,0]
	v_mfma_scale_f32_16x16x128_f8f6f4 v[106:109], v[172:179], v[216:223], v[106:109], v234, v235 op_sel_hi:[0,0,0]
	s_setprio 0
	s_setprio 1
	v_mfma_scale_f32_16x16x128_f8f6f4 v[102:105], v[2:9], v[224:231], v[102:105], v234, v235 op_sel_hi:[0,0,0]
	v_mfma_scale_f32_16x16x128_f8f6f4 v[98:101], v[172:179], v[224:231], v[98:101], v234, v235 op_sel_hi:[0,0,0]
	s_setprio 0
	s_barrier
	s_mov_b32 m0, s7
	v_lshl_add_u64 v[18:19], v[18:19], 0, s[66:67]
	s_add_u32 s44, s44, 0x20080
	ds_read_b128 v[198:201], v196 offset:49152
	ds_read_b128 v[202:205], v196 offset:50176
	ds_read_b128 v[206:209], v196 offset:51200
	ds_read_b128 v[210:213], v196 offset:52224
	ds_read_b128 v[216:219], v196 offset:53248
	ds_read_b128 v[220:223], v196 offset:54272
	ds_read_b128 v[224:227], v196 offset:55296
	ds_read_b128 v[228:231], v196 offset:56320
	global_load_lds_dwordx4 v[18:19], off
	v_lshl_add_u64 v[18:19], v[20:21], 0, s[66:67]
	s_mov_b32 m0, s65
	s_addc_u32 s45, s45, 0
	global_load_lds_dwordx4 v[18:19], off
	v_lshl_add_u64 v[18:19], s[44:45], 0, v[0:1]
	s_mov_b32 m0, s13
	s_nop 0
	global_load_lds_dwordx4 v[18:19], off
	v_lshl_add_u64 v[18:19], s[44:45], 0, v[166:167]
	s_mov_b32 m0, s51
	s_nop 0
	global_load_lds_dwordx4 v[18:19], off
	v_lshl_add_u64 v[18:19], v[22:23], 0, s[66:67]
	s_mov_b32 m0, s68
	s_nop 0
	global_load_lds_dwordx4 v[18:19], off
	v_lshl_add_u64 v[18:19], v[24:25], 0, s[66:67]
	s_mov_b32 m0, s52
	s_nop 0
	global_load_lds_dwordx4 v[18:19], off
	s_waitcnt vmcnt(8)
	s_waitcnt lgkmcnt(0)
	s_barrier
	s_setprio 1
	s_waitcnt lgkmcnt(0)
	v_mfma_scale_f32_16x16x128_f8f6f4 v[94:97], v[10:17], v[198:205], v[94:97], v234, v235 op_sel_hi:[0,0,0]
	v_mfma_scale_f32_16x16x128_f8f6f4 v[90:93], v[26:33], v[198:205], v[90:93], v234, v235 op_sel_hi:[0,0,0]
	s_setprio 0
	s_setprio 1
	v_mfma_scale_f32_16x16x128_f8f6f4 v[86:89], v[10:17], v[206:213], v[86:89], v234, v235 op_sel_hi:[0,0,0]
	v_mfma_scale_f32_16x16x128_f8f6f4 v[82:85], v[26:33], v[206:213], v[82:85], v234, v235 op_sel_hi:[0,0,0]
	s_setprio 0
	s_setprio 1
	v_mfma_scale_f32_16x16x128_f8f6f4 v[78:81], v[10:17], v[216:223], v[78:81], v234, v235 op_sel_hi:[0,0,0]
	v_mfma_scale_f32_16x16x128_f8f6f4 v[74:77], v[26:33], v[216:223], v[74:77], v234, v235 op_sel_hi:[0,0,0]
	s_setprio 0
	s_setprio 1
	v_mfma_scale_f32_16x16x128_f8f6f4 v[70:73], v[10:17], v[224:231], v[70:73], v234, v235 op_sel_hi:[0,0,0]
	v_mfma_scale_f32_16x16x128_f8f6f4 v[66:69], v[26:33], v[224:231], v[66:69], v234, v235 op_sel_hi:[0,0,0]
	s_setprio 0
	s_setprio 1
	v_mfma_scale_f32_16x16x128_f8f6f4 v[62:65], v[2:9], v[198:205], v[62:65], v234, v235 op_sel_hi:[0,0,0]
	v_mfma_scale_f32_16x16x128_f8f6f4 v[58:61], v[172:179], v[198:205], v[58:61], v234, v235 op_sel_hi:[0,0,0]
	s_setprio 0
	s_setprio 1
	v_mfma_scale_f32_16x16x128_f8f6f4 v[54:57], v[2:9], v[206:213], v[54:57], v234, v235 op_sel_hi:[0,0,0]
	v_mfma_scale_f32_16x16x128_f8f6f4 v[50:53], v[172:179], v[206:213], v[50:53], v234, v235 op_sel_hi:[0,0,0]
	s_setprio 0
	s_setprio 1
	v_mfma_scale_f32_16x16x128_f8f6f4 v[46:49], v[2:9], v[216:223], v[46:49], v234, v235 op_sel_hi:[0,0,0]
	v_mfma_scale_f32_16x16x128_f8f6f4 v[42:45], v[172:179], v[216:223], v[42:45], v234, v235 op_sel_hi:[0,0,0]
	s_setprio 0
	s_setprio 1
	v_mfma_scale_f32_16x16x128_f8f6f4 v[38:41], v[2:9], v[224:231], v[38:41], v234, v235 op_sel_hi:[0,0,0]
	v_mfma_scale_f32_16x16x128_f8f6f4 v[34:37], v[172:179], v[224:231], v[34:37], v234, v235 op_sel_hi:[0,0,0]
	s_setprio 0
	s_barrier
	s_add_i32 s75, s75, 2
	s_add_u32 s46, s46, 0x100
	s_addc_u32 s47, s47, 0
	s_add_u32 s37, s37, 0x100
	s_addc_u32 s74, s74, 0
	s_cmp_gt_u32 s75, 5
	s_cbranch_scc0 .LBB0_388
	s_and_b64 vcc, exec, s[30:31]
	s_cbranch_vccz .LBB0_391
	s_barrier

.LBB0_1368:
	v_add_u32_e32 v134, 0x10000, v226
	v_add_u32_e32 v146, 0x14000, v226
	ds_read_b128 v[150:153], v134
	ds_read_b128 v[154:157], v134 offset:1024
	ds_read_b128 v[158:161], v134 offset:2048
	ds_read_b128 v[162:165], v134 offset:3072
	s_waitcnt vmcnt(0)
	ds_read_b128 v[134:137], v146
	ds_read_b128 v[138:141], v146 offset:1024
	ds_read_b128 v[142:145], v146 offset:2048
	ds_read_b128 v[146:149], v146 offset:3072
	v_lshl_add_u64 v[208:209], s[44:45], 0, v[204:205]
	s_add_i32 m0, s52, 0xc000
	s_waitcnt lgkmcnt(0)
	ds_read_b128 v[178:181], v227
	ds_read_b128 v[194:197], v227 offset:1024
	ds_read_b128 v[174:177], v227 offset:2048
	ds_read_b128 v[190:193], v227 offset:3072
	ds_read_b128 v[170:173], v227 offset:4096
	ds_read_b128 v[186:189], v227 offset:5120
	ds_read_b128 v[166:169], v227 offset:6144
	ds_read_b128 v[182:185], v227 offset:7168
	global_load_lds_dwordx4 v[208:209], off
	v_lshl_add_u64 v[208:209], s[44:45], 0, v[206:207]
	s_add_i32 m0, s52, 0xe000
	s_nop 0
	global_load_lds_dwordx4 v[208:209], off
	s_waitcnt vmcnt(8)
	s_waitcnt lgkmcnt(0)
	s_barrier
	s_setprio 1
	s_waitcnt lgkmcnt(0)
	v_mfma_f32_16x16x32_bf16 v[130:133], v[150:153], v[178:181], v[130:133]
	v_mfma_f32_16x16x32_bf16 v[126:129], v[158:161], v[178:181], v[126:129]
	v_mfma_f32_16x16x32_bf16 v[122:125], v[150:153], v[174:177], v[122:125]
	v_mfma_f32_16x16x32_bf16 v[118:121], v[158:161], v[174:177], v[118:121]
	s_setprio 0
	s_setprio 1
	v_mfma_f32_16x16x32_bf16 v[114:117], v[150:153], v[170:173], v[114:117]
	v_mfma_f32_16x16x32_bf16 v[110:113], v[158:161], v[170:173], v[110:113]
	v_mfma_f32_16x16x32_bf16 v[106:109], v[150:153], v[166:169], v[106:109]
	v_mfma_f32_16x16x32_bf16 v[102:105], v[158:161], v[166:169], v[102:105]
	s_setprio 0
	s_setprio 1
	v_mfma_f32_16x16x32_bf16 v[130:133], v[154:157], v[194:197], v[130:133]
	v_mfma_f32_16x16x32_bf16 v[126:129], v[162:165], v[194:197], v[126:129]
	v_mfma_f32_16x16x32_bf16 v[122:125], v[154:157], v[190:193], v[122:125]
	v_mfma_f32_16x16x32_bf16 v[118:121], v[162:165], v[190:193], v[118:121]
	s_setprio 0
	s_setprio 1
	v_mfma_f32_16x16x32_bf16 v[114:117], v[154:157], v[186:189], v[114:117]
	v_mfma_f32_16x16x32_bf16 v[110:113], v[162:165], v[186:189], v[110:113]
	v_mfma_f32_16x16x32_bf16 v[106:109], v[154:157], v[182:185], v[106:109]
	v_mfma_f32_16x16x32_bf16 v[102:105], v[162:165], v[182:185], v[102:105]
	s_setprio 0
	s_setprio 1
	v_mfma_f32_16x16x32_bf16 v[98:101], v[134:137], v[178:181], v[98:101]
	v_mfma_f32_16x16x32_bf16 v[94:97], v[142:145], v[178:181], v[94:97]
	v_mfma_f32_16x16x32_bf16 v[90:93], v[134:137], v[174:177], v[90:93]
	v_mfma_f32_16x16x32_bf16 v[86:89], v[142:145], v[174:177], v[86:89]
	s_setprio 0
	s_setprio 1
	v_mfma_f32_16x16x32_bf16 v[82:85], v[134:137], v[170:173], v[82:85]
	v_mfma_f32_16x16x32_bf16 v[78:81], v[142:145], v[170:173], v[78:81]
	v_mfma_f32_16x16x32_bf16 v[74:77], v[134:137], v[166:169], v[74:77]
	v_mfma_f32_16x16x32_bf16 v[70:73], v[142:145], v[166:169], v[70:73]
	s_setprio 0
	s_setprio 1
	v_mfma_f32_16x16x32_bf16 v[98:101], v[138:141], v[194:197], v[98:101]
	v_mfma_f32_16x16x32_bf16 v[94:97], v[146:149], v[194:197], v[94:97]
	v_mfma_f32_16x16x32_bf16 v[90:93], v[138:141], v[190:193], v[90:93]
	v_mfma_f32_16x16x32_bf16 v[86:89], v[146:149], v[190:193], v[86:89]
	s_setprio 0
	s_setprio 1
	v_mfma_f32_16x16x32_bf16 v[82:85], v[138:141], v[186:189], v[82:85]
	v_mfma_f32_16x16x32_bf16 v[78:81], v[146:149], v[186:189], v[78:81]
	v_mfma_f32_16x16x32_bf16 v[74:77], v[138:141], v[182:185], v[74:77]
	v_mfma_f32_16x16x32_bf16 v[70:73], v[146:149], v[182:185], v[70:73]
	s_setprio 0
	s_barrier
	v_cndmask_b32_e64 v208, 0, 1, s[6:7]
	v_cmp_ne_u32_e64 s[8:9], 1, v208
	s_andn2_b64 vcc, exec, s[6:7]
	s_cbranch_vccnz .LBB0_1370
	ds_read_b128 v[178:181], v227 offset:16384
	ds_read_b128 v[194:197], v227 offset:17408
	ds_read_b128 v[174:177], v227 offset:18432
	ds_read_b128 v[190:193], v227 offset:19456
	ds_read_b128 v[170:173], v227 offset:20480
	ds_read_b128 v[186:189], v227 offset:21504
	ds_read_b128 v[166:169], v227 offset:22528
	ds_read_b128 v[182:185], v227 offset:23552
.LBB0_1370:
	s_add_u32 s46, s44, 0xfffa0080
	s_addc_u32 s47, s45, -1
	s_cmp_eq_u32 s83, 4
	s_cselect_b32 s49, s41, s47
	s_cselect_b32 s48, s40, s46
	s_cselect_b32 s47, s27, s75
	s_cselect_b32 s46, s39, s74
	s_mov_b32 m0, s53
	v_lshl_add_u64 v[208:209], s[46:47], 0, v[0:1]
	s_add_u32 vcc_lo, s46, 0x20000
	global_load_lds_dwordx4 v[208:209], off
	v_lshl_add_u64 v[210:211], s[46:47], 0, v[202:203]
	s_mov_b32 m0, s54
	s_addc_u32 vcc_hi, s47, 0
	global_load_lds_dwordx4 v[210:211], off
	v_lshl_add_u64 v[212:213], vcc, 0, v[0:1]
	s_mov_b32 m0, s55
	v_lshl_add_u64 v[216:217], s[48:49], 0, v[200:201]
	global_load_lds_dwordx4 v[212:213], off
	v_lshl_add_u64 v[212:213], vcc, 0, v[202:203]
	s_mov_b32 m0, s56
	s_and_b64 vcc, exec, s[8:9]
	global_load_lds_dwordx4 v[212:213], off
	v_lshl_add_u64 v[212:213], s[48:49], 0, v[198:199]
	s_mov_b32 m0, s52
	s_nop 0
	global_load_lds_dwordx4 v[212:213], off
	s_mov_b32 m0, s57
	s_nop 0
	global_load_lds_dwordx4 v[216:217], off
	s_waitcnt vmcnt(8)
	s_waitcnt lgkmcnt(0)
	s_barrier
	s_cbranch_vccnz .LBB0_1372
	s_setprio 1
	s_waitcnt lgkmcnt(0)
	v_mfma_f32_16x16x32_bf16 v[66:69], v[150:153], v[178:181], v[66:69]
	v_mfma_f32_16x16x32_bf16 v[62:65], v[158:161], v[178:181], v[62:65]
	v_mfma_f32_16x16x32_bf16 v[58:61], v[150:153], v[174:177], v[58:61]
	v_mfma_f32_16x16x32_bf16 v[54:57], v[158:161], v[174:177], v[54:57]
	s_setprio 0
	s_setprio 1
	v_mfma_f32_16x16x32_bf16 v[50:53], v[150:153], v[170:173], v[50:53]
	v_mfma_f32_16x16x32_bf16 v[46:49], v[158:161], v[170:173], v[46:49]
	v_mfma_f32_16x16x32_bf16 v[42:45], v[150:153], v[166:169], v[42:45]
	v_mfma_f32_16x16x32_bf16 v[38:41], v[158:161], v[166:169], v[38:41]
	s_setprio 0
	s_setprio 1
	v_mfma_f32_16x16x32_bf16 v[66:69], v[154:157], v[194:197], v[66:69]
	v_mfma_f32_16x16x32_bf16 v[62:65], v[162:165], v[194:197], v[62:65]
	v_mfma_f32_16x16x32_bf16 v[58:61], v[154:157], v[190:193], v[58:61]
	v_mfma_f32_16x16x32_bf16 v[54:57], v[162:165], v[190:193], v[54:57]
	s_setprio 0
	s_setprio 1
	v_mfma_f32_16x16x32_bf16 v[50:53], v[154:157], v[186:189], v[50:53]
	v_mfma_f32_16x16x32_bf16 v[46:49], v[162:165], v[186:189], v[46:49]
	v_mfma_f32_16x16x32_bf16 v[42:45], v[154:157], v[182:185], v[42:45]
	v_mfma_f32_16x16x32_bf16 v[38:41], v[162:165], v[182:185], v[38:41]
	s_setprio 0
	s_setprio 1
	v_mfma_f32_16x16x32_bf16 v[34:37], v[134:137], v[178:181], v[34:37]
	v_mfma_f32_16x16x32_bf16 v[30:33], v[142:145], v[178:181], v[30:33]
	v_mfma_f32_16x16x32_bf16 v[26:29], v[134:137], v[174:177], v[26:29]
	v_mfma_f32_16x16x32_bf16 v[22:25], v[142:145], v[174:177], v[22:25]
	s_setprio 0
	s_setprio 1
	v_mfma_f32_16x16x32_bf16 v[18:21], v[134:137], v[170:173], v[18:21]
	v_mfma_f32_16x16x32_bf16 v[14:17], v[142:145], v[170:173], v[14:17]
	v_mfma_f32_16x16x32_bf16 v[10:13], v[134:137], v[166:169], v[10:13]
	v_mfma_f32_16x16x32_bf16 v[6:9], v[142:145], v[166:169], v[6:9]
	s_setprio 0
	s_setprio 1
	v_mfma_f32_16x16x32_bf16 v[34:37], v[138:141], v[194:197], v[34:37]
	v_mfma_f32_16x16x32_bf16 v[30:33], v[146:149], v[194:197], v[30:33]
	v_mfma_f32_16x16x32_bf16 v[26:29], v[138:141], v[190:193], v[26:29]
	v_mfma_f32_16x16x32_bf16 v[22:25], v[146:149], v[190:193], v[22:25]
	s_setprio 0
	s_setprio 1
	v_mfma_f32_16x16x32_bf16 v[18:21], v[138:141], v[186:189], v[18:21]
	v_mfma_f32_16x16x32_bf16 v[14:17], v[146:149], v[186:189], v[14:17]
	v_mfma_f32_16x16x32_bf16 v[10:13], v[138:141], v[182:185], v[10:13]
	v_mfma_f32_16x16x32_bf16 v[6:9], v[146:149], v[182:185], v[6:9]
	s_setprio 0
.LBB0_1372:
	s_barrier
	v_add_u32_e32 v134, 0x18000, v226
	v_add_u32_e32 v146, 0x1c000, v226
	ds_read_b128 v[150:153], v134
	ds_read_b128 v[154:157], v134 offset:1024
	ds_read_b128 v[158:161], v134 offset:2048
	ds_read_b128 v[162:165], v134 offset:3072
	ds_read_b128 v[134:137], v146
	ds_read_b128 v[138:141], v146 offset:1024
	ds_read_b128 v[142:145], v146 offset:2048
	ds_read_b128 v[146:149], v146 offset:3072
	s_add_u32 s48, s48, 0x60000
	s_addc_u32 s49, s49, 0
	s_mov_b32 m0, s58
	v_lshl_add_u64 v[218:219], s[48:49], 0, v[198:199]
	s_waitcnt lgkmcnt(0)
	ds_read_b128 v[178:181], v227 offset:32768
	ds_read_b128 v[194:197], v227 offset:33792
	ds_read_b128 v[174:177], v227 offset:34816
	ds_read_b128 v[190:193], v227 offset:35840
	ds_read_b128 v[170:173], v227 offset:36864
	ds_read_b128 v[186:189], v227 offset:37888
	ds_read_b128 v[166:169], v227 offset:38912
	ds_read_b128 v[182:185], v227 offset:39936
	global_load_lds_dwordx4 v[218:219], off
	v_lshl_add_u64 v[218:219], s[48:49], 0, v[200:201]
	s_mov_b32 m0, s59
	s_nop 0
	global_load_lds_dwordx4 v[218:219], off
	s_waitcnt vmcnt(8)
	s_waitcnt lgkmcnt(0)
	s_barrier
	s_setprio 1
	s_waitcnt lgkmcnt(0)
	v_mfma_f32_16x16x32_bf16 v[130:133], v[150:153], v[178:181], v[130:133]
	v_mfma_f32_16x16x32_bf16 v[126:129], v[158:161], v[178:181], v[126:129]
	v_mfma_f32_16x16x32_bf16 v[122:125], v[150:153], v[174:177], v[122:125]
	v_mfma_f32_16x16x32_bf16 v[118:121], v[158:161], v[174:177], v[118:121]
	s_setprio 0
	s_setprio 1
	v_mfma_f32_16x16x32_bf16 v[114:117], v[150:153], v[170:173], v[114:117]
	v_mfma_f32_16x16x32_bf16 v[110:113], v[158:161], v[170:173], v[110:113]
	v_mfma_f32_16x16x32_bf16 v[106:109], v[150:153], v[166:169], v[106:109]
	v_mfma_f32_16x16x32_bf16 v[102:105], v[158:161], v[166:169], v[102:105]
	s_setprio 0
	s_setprio 1
	v_mfma_f32_16x16x32_bf16 v[130:133], v[154:157], v[194:197], v[130:133]
	v_mfma_f32_16x16x32_bf16 v[126:129], v[162:165], v[194:197], v[126:129]
	v_mfma_f32_16x16x32_bf16 v[122:125], v[154:157], v[190:193], v[122:125]
	v_mfma_f32_16x16x32_bf16 v[118:121], v[162:165], v[190:193], v[118:121]
	s_setprio 0
	s_setprio 1
	v_mfma_f32_16x16x32_bf16 v[114:117], v[154:157], v[186:189], v[114:117]
	v_mfma_f32_16x16x32_bf16 v[110:113], v[162:165], v[186:189], v[110:113]
	v_mfma_f32_16x16x32_bf16 v[106:109], v[154:157], v[182:185], v[106:109]
	v_mfma_f32_16x16x32_bf16 v[102:105], v[162:165], v[182:185], v[102:105]
	s_setprio 0
	s_setprio 1
	v_mfma_f32_16x16x32_bf16 v[98:101], v[134:137], v[178:181], v[98:101]
	v_mfma_f32_16x16x32_bf16 v[94:97], v[142:145], v[178:181], v[94:97]
	v_mfma_f32_16x16x32_bf16 v[90:93], v[134:137], v[174:177], v[90:93]
	v_mfma_f32_16x16x32_bf16 v[86:89], v[142:145], v[174:177], v[86:89]
	s_setprio 0
	s_setprio 1
	v_mfma_f32_16x16x32_bf16 v[82:85], v[134:137], v[170:173], v[82:85]
	v_mfma_f32_16x16x32_bf16 v[78:81], v[142:145], v[170:173], v[78:81]
	v_mfma_f32_16x16x32_bf16 v[74:77], v[134:137], v[166:169], v[74:77]
	v_mfma_f32_16x16x32_bf16 v[70:73], v[142:145], v[166:169], v[70:73]
	s_setprio 0
	s_setprio 1
	v_mfma_f32_16x16x32_bf16 v[98:101], v[138:141], v[194:197], v[98:101]
	v_mfma_f32_16x16x32_bf16 v[94:97], v[146:149], v[194:197], v[94:97]
	v_mfma_f32_16x16x32_bf16 v[90:93], v[138:141], v[190:193], v[90:93]
	v_mfma_f32_16x16x32_bf16 v[86:89], v[146:149], v[190:193], v[86:89]
	s_setprio 0
	s_setprio 1
	v_mfma_f32_16x16x32_bf16 v[82:85], v[138:141], v[186:189], v[82:85]
	v_mfma_f32_16x16x32_bf16 v[78:81], v[146:149], v[186:189], v[78:81]
	v_mfma_f32_16x16x32_bf16 v[74:77], v[138:141], v[182:185], v[74:77]
	v_mfma_f32_16x16x32_bf16 v[70:73], v[146:149], v[182:185], v[70:73]
	s_setprio 0
	s_barrier
	s_and_b64 vcc, exec, s[8:9]
	s_cbranch_vccnz .LBB0_1374
	ds_read_b128 v[178:181], v227 offset:49152
	ds_read_b128 v[194:197], v227 offset:50176
	ds_read_b128 v[174:177], v227 offset:51200
	ds_read_b128 v[190:193], v227 offset:52224
	ds_read_b128 v[170:173], v227 offset:53248
	ds_read_b128 v[186:189], v227 offset:54272
	ds_read_b128 v[166:169], v227 offset:55296
	ds_read_b128 v[182:185], v227 offset:56320
.LBB0_1374:
	s_mov_b32 m0, s62
	v_lshl_add_u64 v[208:209], v[208:209], 0, s[66:67]
	s_add_u32 s46, s46, 0x20080
	global_load_lds_dwordx4 v[208:209], off
	v_lshl_add_u64 v[208:209], v[210:211], 0, s[66:67]
	s_mov_b32 m0, s63
	s_addc_u32 s47, s47, 0
	global_load_lds_dwordx4 v[208:209], off
	v_lshl_add_u64 v[208:209], s[46:47], 0, v[0:1]
	s_mov_b32 m0, s68
	s_and_b64 vcc, exec, s[8:9]
	global_load_lds_dwordx4 v[208:209], off
	v_lshl_add_u64 v[208:209], s[46:47], 0, v[202:203]
	s_mov_b32 m0, s81
	s_nop 0
	global_load_lds_dwordx4 v[208:209], off
	v_lshl_add_u64 v[208:209], v[212:213], 0, s[66:67]
	s_mov_b32 m0, s64
	s_nop 0
	global_load_lds_dwordx4 v[208:209], off
	v_lshl_add_u64 v[208:209], v[216:217], 0, s[66:67]
	s_mov_b32 m0, s65
	s_nop 0
	global_load_lds_dwordx4 v[208:209], off
	s_waitcnt vmcnt(8)
	s_waitcnt lgkmcnt(0)
	s_barrier
	s_cbranch_vccnz .LBB0_1367
	s_setprio 1
	s_waitcnt lgkmcnt(0)
	v_mfma_f32_16x16x32_bf16 v[66:69], v[150:153], v[178:181], v[66:69]
	v_mfma_f32_16x16x32_bf16 v[62:65], v[158:161], v[178:181], v[62:65]
	v_mfma_f32_16x16x32_bf16 v[58:61], v[150:153], v[174:177], v[58:61]
	v_mfma_f32_16x16x32_bf16 v[54:57], v[158:161], v[174:177], v[54:57]
	s_setprio 0
	s_setprio 1
	v_mfma_f32_16x16x32_bf16 v[50:53], v[150:153], v[170:173], v[50:53]
	v_mfma_f32_16x16x32_bf16 v[46:49], v[158:161], v[170:173], v[46:49]
	v_mfma_f32_16x16x32_bf16 v[42:45], v[150:153], v[166:169], v[42:45]
	v_mfma_f32_16x16x32_bf16 v[38:41], v[158:161], v[166:169], v[38:41]
	s_setprio 0
	s_setprio 1
	v_mfma_f32_16x16x32_bf16 v[66:69], v[154:157], v[194:197], v[66:69]
	v_mfma_f32_16x16x32_bf16 v[62:65], v[162:165], v[194:197], v[62:65]
	v_mfma_f32_16x16x32_bf16 v[58:61], v[154:157], v[190:193], v[58:61]
	v_mfma_f32_16x16x32_bf16 v[54:57], v[162:165], v[190:193], v[54:57]
	s_setprio 0
	s_setprio 1
	v_mfma_f32_16x16x32_bf16 v[50:53], v[154:157], v[186:189], v[50:53]
	v_mfma_f32_16x16x32_bf16 v[46:49], v[162:165], v[186:189], v[46:49]
	v_mfma_f32_16x16x32_bf16 v[42:45], v[154:157], v[182:185], v[42:45]
	v_mfma_f32_16x16x32_bf16 v[38:41], v[162:165], v[182:185], v[38:41]
	s_setprio 0
	s_setprio 1
	v_mfma_f32_16x16x32_bf16 v[34:37], v[134:137], v[178:181], v[34:37]
	v_mfma_f32_16x16x32_bf16 v[30:33], v[142:145], v[178:181], v[30:33]
	v_mfma_f32_16x16x32_bf16 v[26:29], v[134:137], v[174:177], v[26:29]
	v_mfma_f32_16x16x32_bf16 v[22:25], v[142:145], v[174:177], v[22:25]
	s_setprio 0
	s_setprio 1
	v_mfma_f32_16x16x32_bf16 v[18:21], v[134:137], v[170:173], v[18:21]
	v_mfma_f32_16x16x32_bf16 v[14:17], v[142:145], v[170:173], v[14:17]
	v_mfma_f32_16x16x32_bf16 v[10:13], v[134:137], v[166:169], v[10:13]
	v_mfma_f32_16x16x32_bf16 v[6:9], v[142:145], v[166:169], v[6:9]
	s_setprio 0
	s_setprio 1
	v_mfma_f32_16x16x32_bf16 v[34:37], v[138:141], v[194:197], v[34:37]
	v_mfma_f32_16x16x32_bf16 v[30:33], v[146:149], v[194:197], v[30:33]
	v_mfma_f32_16x16x32_bf16 v[26:29], v[138:141], v[190:193], v[26:29]
	v_mfma_f32_16x16x32_bf16 v[22:25], v[146:149], v[190:193], v[22:25]
	s_setprio 0
	s_setprio 1
	v_mfma_f32_16x16x32_bf16 v[18:21], v[138:141], v[186:189], v[18:21]
	v_mfma_f32_16x16x32_bf16 v[14:17], v[146:149], v[186:189], v[14:17]
	v_mfma_f32_16x16x32_bf16 v[10:13], v[138:141], v[182:185], v[10:13]
	v_mfma_f32_16x16x32_bf16 v[6:9], v[146:149], v[182:185], v[6:9]
	s_setprio 0
	s_branch .LBB0_1367

.LBB0_1556:
	v_add_u32_e32 v54, 0x10000, v247
	ds_read_b128 v[166:169], v54
	ds_read_b128 v[170:173], v54 offset:1024
	ds_read_b128 v[174:177], v54 offset:2048
	ds_read_b128 v[178:181], v54 offset:3072
	v_add_u32_e32 v54, 0x14000, v247
	ds_read_b128 v[150:153], v54
	ds_read_b128 v[154:157], v54 offset:1024
	ds_read_b128 v[158:161], v54 offset:2048
	ds_read_b128 v[162:165], v54 offset:3072
	v_lshl_add_u64 v[54:55], s[40:41], 0, v[222:223]
	s_add_i32 m0, s26, 0xc000
	s_waitcnt lgkmcnt(0)
	ds_read_b128 v[194:197], v248
	ds_read_b128 v[210:213], v248 offset:1024
	ds_read_b128 v[190:193], v248 offset:2048
	ds_read_b128 v[206:209], v248 offset:3072
	ds_read_b128 v[186:189], v248 offset:4096
	ds_read_b128 v[202:205], v248 offset:5120
	ds_read_b128 v[182:185], v248 offset:6144
	ds_read_b128 v[198:201], v248 offset:7168
	global_load_lds_dwordx4 v[54:55], off
	v_lshl_add_u64 v[54:55], s[40:41], 0, v[224:225]
	s_add_i32 m0, s26, 0xe000
	s_nop 0
	global_load_lds_dwordx4 v[54:55], off
	s_waitcnt vmcnt(8)
	s_waitcnt lgkmcnt(0)
	s_barrier
	s_setprio 1
	s_waitcnt lgkmcnt(0)
	v_mfma_f32_16x16x32_bf16 v[54:57], v[166:169], v[194:197], v[146:149]
	v_mfma_f32_16x16x32_bf16 v[58:61], v[174:177], v[194:197], v[142:145]
	v_mfma_f32_16x16x32_bf16 v[66:69], v[166:169], v[190:193], v[130:133]
	v_mfma_f32_16x16x32_bf16 v[74:77], v[174:177], v[190:193], v[126:129]
	s_setprio 0
	s_setprio 1
	v_mfma_f32_16x16x32_bf16 v[114:117], v[166:169], v[186:189], v[114:117]
	v_mfma_f32_16x16x32_bf16 v[110:113], v[174:177], v[186:189], v[110:113]
	v_mfma_f32_16x16x32_bf16 v[98:101], v[166:169], v[182:185], v[98:101]
	v_mfma_f32_16x16x32_bf16 v[94:97], v[174:177], v[182:185], v[94:97]
	s_setprio 0
	s_setprio 1
	v_mfma_f32_16x16x32_bf16 v[54:57], v[170:173], v[210:213], v[54:57]
	v_mfma_f32_16x16x32_bf16 v[58:61], v[178:181], v[210:213], v[58:61]
	v_mfma_f32_16x16x32_bf16 v[66:69], v[170:173], v[206:209], v[66:69]
	v_mfma_f32_16x16x32_bf16 v[74:77], v[178:181], v[206:209], v[74:77]
	s_setprio 0
	s_setprio 1
	v_mfma_f32_16x16x32_bf16 v[114:117], v[170:173], v[202:205], v[114:117]
	v_mfma_f32_16x16x32_bf16 v[110:113], v[178:181], v[202:205], v[110:113]
	v_mfma_f32_16x16x32_bf16 v[98:101], v[170:173], v[198:201], v[98:101]
	v_mfma_f32_16x16x32_bf16 v[94:97], v[178:181], v[198:201], v[94:97]
	s_setprio 0
	s_setprio 1
	v_mfma_f32_16x16x32_bf16 v[126:129], v[150:153], v[194:197], v[138:141]
	v_mfma_f32_16x16x32_bf16 v[138:141], v[154:157], v[210:213], v[126:129]
	v_mfma_f32_16x16x32_bf16 v[126:129], v[158:161], v[194:197], v[134:137]
	v_mfma_f32_16x16x32_bf16 v[122:125], v[150:153], v[190:193], v[122:125]
	s_setprio 0
	s_setprio 1
	v_mfma_f32_16x16x32_bf16 v[118:121], v[158:161], v[190:193], v[118:121]
	v_mfma_f32_16x16x32_bf16 v[106:109], v[150:153], v[186:189], v[106:109]
	v_mfma_f32_16x16x32_bf16 v[102:105], v[158:161], v[186:189], v[102:105]
	v_mfma_f32_16x16x32_bf16 v[90:93], v[150:153], v[182:185], v[90:93]
	s_setprio 0
	s_setprio 1
	v_mfma_f32_16x16x32_bf16 v[86:89], v[158:161], v[182:185], v[86:89]
	v_mfma_f32_16x16x32_bf16 v[134:137], v[162:165], v[210:213], v[126:129]
	v_mfma_f32_16x16x32_bf16 v[122:125], v[154:157], v[206:209], v[122:125]
	v_mfma_f32_16x16x32_bf16 v[118:121], v[162:165], v[206:209], v[118:121]
	s_setprio 0
	s_setprio 1
	v_mfma_f32_16x16x32_bf16 v[106:109], v[154:157], v[202:205], v[106:109]
	v_mfma_f32_16x16x32_bf16 v[102:105], v[162:165], v[202:205], v[102:105]
	v_mfma_f32_16x16x32_bf16 v[90:93], v[154:157], v[198:201], v[90:93]
	v_mfma_f32_16x16x32_bf16 v[86:89], v[162:165], v[198:201], v[86:89]
	s_setprio 0
	s_barrier
	v_cndmask_b32_e64 v126, 0, 1, s[38:39]
	v_cmp_ne_u32_e64 s[0:1], 1, v126
	s_andn2_b64 vcc, exec, s[38:39]
	s_cbranch_vccnz .LBB0_1558
	ds_read_b128 v[194:197], v248 offset:16384
	ds_read_b128 v[210:213], v248 offset:17408
	ds_read_b128 v[190:193], v248 offset:18432
	ds_read_b128 v[206:209], v248 offset:19456
	ds_read_b128 v[186:189], v248 offset:20480
	ds_read_b128 v[202:205], v248 offset:21504
	ds_read_b128 v[182:185], v248 offset:22528
	ds_read_b128 v[198:201], v248 offset:23552
.LBB0_1558:
	s_add_u32 s42, s40, 0xfffc0080
	s_addc_u32 s43, s41, -1
	s_cmp_eq_u32 s90, 12
	s_cselect_b32 s45, s74, s43
	s_cselect_b32 s44, s75, s42
	s_cselect_b32 s43, s11, s88
	s_cselect_b32 s42, s81, s83
	s_mov_b32 m0, s27
	v_lshl_add_u64 v[226:227], s[42:43], 0, v[0:1]
	s_add_u32 vcc_lo, s42, 0x40000
	global_load_lds_dwordx4 v[226:227], off
	v_lshl_add_u64 v[228:229], s[42:43], 0, v[220:221]
	s_mov_b32 m0, s37
	s_addc_u32 vcc_hi, s43, 0
	global_load_lds_dwordx4 v[228:229], off
	v_lshl_add_u64 v[126:127], vcc, 0, v[0:1]
	s_mov_b32 m0, s47
	v_lshl_add_u64 v[230:231], s[44:45], 0, v[216:217]
	global_load_lds_dwordx4 v[126:127], off
	v_lshl_add_u64 v[126:127], vcc, 0, v[220:221]
	s_mov_b32 m0, s48
	v_lshl_add_u64 v[232:233], s[44:45], 0, v[218:219]
	global_load_lds_dwordx4 v[126:127], off
	s_mov_b32 m0, s26
	s_and_b64 vcc, exec, s[0:1]
	global_load_lds_dwordx4 v[230:231], off
	s_mov_b32 m0, s49
	s_nop 0
	global_load_lds_dwordx4 v[232:233], off
	s_waitcnt vmcnt(8)
	s_waitcnt lgkmcnt(0)
	s_barrier
	s_cbranch_vccnz .LBB0_1560
	s_setprio 1
	s_waitcnt lgkmcnt(0)
	v_mfma_f32_16x16x32_bf16 v[82:85], v[166:169], v[194:197], v[82:85]
	v_mfma_f32_16x16x32_bf16 v[78:81], v[174:177], v[194:197], v[78:81]
	v_mfma_f32_16x16x32_bf16 v[50:53], v[166:169], v[190:193], v[50:53]
	v_mfma_f32_16x16x32_bf16 v[46:49], v[174:177], v[190:193], v[46:49]
	s_setprio 0
	s_setprio 1
	v_mfma_f32_16x16x32_bf16 v[34:37], v[166:169], v[186:189], v[34:37]
	v_mfma_f32_16x16x32_bf16 v[30:33], v[174:177], v[186:189], v[30:33]
	v_mfma_f32_16x16x32_bf16 v[18:21], v[166:169], v[182:185], v[18:21]
	v_mfma_f32_16x16x32_bf16 v[14:17], v[174:177], v[182:185], v[14:17]
	s_setprio 0
	s_setprio 1
	v_mfma_f32_16x16x32_bf16 v[82:85], v[170:173], v[210:213], v[82:85]
	v_mfma_f32_16x16x32_bf16 v[78:81], v[178:181], v[210:213], v[78:81]
	v_mfma_f32_16x16x32_bf16 v[50:53], v[170:173], v[206:209], v[50:53]
	v_mfma_f32_16x16x32_bf16 v[46:49], v[178:181], v[206:209], v[46:49]
	s_setprio 0
	s_setprio 1
	v_mfma_f32_16x16x32_bf16 v[34:37], v[170:173], v[202:205], v[34:37]
	v_mfma_f32_16x16x32_bf16 v[30:33], v[178:181], v[202:205], v[30:33]
	v_mfma_f32_16x16x32_bf16 v[18:21], v[170:173], v[198:201], v[18:21]
	v_mfma_f32_16x16x32_bf16 v[14:17], v[178:181], v[198:201], v[14:17]
	s_setprio 0
	s_setprio 1
	v_mfma_f32_16x16x32_bf16 v[70:73], v[150:153], v[194:197], v[70:73]
	v_mfma_f32_16x16x32_bf16 v[62:65], v[158:161], v[194:197], v[62:65]
	v_mfma_f32_16x16x32_bf16 v[42:45], v[150:153], v[190:193], v[42:45]
	v_mfma_f32_16x16x32_bf16 v[38:41], v[158:161], v[190:193], v[38:41]
	s_setprio 0
	s_setprio 1
	v_mfma_f32_16x16x32_bf16 v[26:29], v[150:153], v[186:189], v[26:29]
	v_mfma_f32_16x16x32_bf16 v[22:25], v[158:161], v[186:189], v[22:25]
	v_mfma_f32_16x16x32_bf16 v[10:13], v[150:153], v[182:185], v[10:13]
	v_mfma_f32_16x16x32_bf16 v[6:9], v[158:161], v[182:185], v[6:9]
	s_setprio 0
	s_setprio 1
	v_mfma_f32_16x16x32_bf16 v[70:73], v[154:157], v[210:213], v[70:73]
	v_mfma_f32_16x16x32_bf16 v[62:65], v[162:165], v[210:213], v[62:65]
	v_mfma_f32_16x16x32_bf16 v[42:45], v[154:157], v[206:209], v[42:45]
	v_mfma_f32_16x16x32_bf16 v[38:41], v[162:165], v[206:209], v[38:41]
	s_setprio 0
	s_setprio 1
	v_mfma_f32_16x16x32_bf16 v[26:29], v[154:157], v[202:205], v[26:29]
	v_mfma_f32_16x16x32_bf16 v[22:25], v[162:165], v[202:205], v[22:25]
	v_mfma_f32_16x16x32_bf16 v[10:13], v[154:157], v[198:201], v[10:13]
	v_mfma_f32_16x16x32_bf16 v[6:9], v[162:165], v[198:201], v[6:9]
	s_setprio 0
.LBB0_1560:
	s_barrier
	v_add_u32_e32 v126, 0x18000, v247
	ds_read_b128 v[166:169], v126
	ds_read_b128 v[170:173], v126 offset:1024
	ds_read_b128 v[174:177], v126 offset:2048
	ds_read_b128 v[178:181], v126 offset:3072
	v_add_u32_e32 v126, 0x1c000, v247
	ds_read_b128 v[150:153], v126
	ds_read_b128 v[154:157], v126 offset:1024
	ds_read_b128 v[158:161], v126 offset:2048
	ds_read_b128 v[162:165], v126 offset:3072
	s_add_u32 s44, s44, 0x40000
	s_addc_u32 s45, s45, 0
	s_mov_b32 m0, s50
	v_lshl_add_u64 v[126:127], s[44:45], 0, v[216:217]
	s_waitcnt lgkmcnt(0)
	ds_read_b128 v[194:197], v248 offset:32768
	ds_read_b128 v[210:213], v248 offset:33792
	ds_read_b128 v[190:193], v248 offset:34816
	ds_read_b128 v[206:209], v248 offset:35840
	ds_read_b128 v[186:189], v248 offset:36864
	ds_read_b128 v[202:205], v248 offset:37888
	ds_read_b128 v[182:185], v248 offset:38912
	ds_read_b128 v[198:201], v248 offset:39936
	global_load_lds_dwordx4 v[126:127], off
	v_lshl_add_u64 v[126:127], s[44:45], 0, v[218:219]
	s_mov_b32 m0, s51
	s_nop 0
	global_load_lds_dwordx4 v[126:127], off
	s_waitcnt vmcnt(8)
	s_waitcnt lgkmcnt(0)
	s_barrier
	s_setprio 1
	s_waitcnt lgkmcnt(0)
	v_mfma_f32_16x16x32_bf16 v[54:57], v[166:169], v[194:197], v[54:57]
	v_mfma_f32_16x16x32_bf16 v[146:149], v[170:173], v[210:213], v[54:57]
	v_mfma_f32_16x16x32_bf16 v[54:57], v[174:177], v[194:197], v[58:61]
	v_mfma_f32_16x16x32_bf16 v[142:145], v[178:181], v[210:213], v[54:57]
	s_setprio 0
	s_setprio 1
	v_mfma_f32_16x16x32_bf16 v[54:57], v[166:169], v[190:193], v[66:69]
	v_mfma_f32_16x16x32_bf16 v[130:133], v[170:173], v[206:209], v[54:57]
	v_mfma_f32_16x16x32_bf16 v[54:57], v[174:177], v[190:193], v[74:77]
	v_mfma_f32_16x16x32_bf16 v[126:129], v[178:181], v[206:209], v[54:57]
	s_setprio 0
	s_setprio 1
	v_mfma_f32_16x16x32_bf16 v[54:57], v[166:169], v[186:189], v[114:117]
	v_mfma_f32_16x16x32_bf16 v[114:117], v[170:173], v[202:205], v[54:57]
	v_mfma_f32_16x16x32_bf16 v[54:57], v[174:177], v[186:189], v[110:113]
	v_mfma_f32_16x16x32_bf16 v[110:113], v[178:181], v[202:205], v[54:57]
	s_setprio 0
	s_setprio 1
	v_mfma_f32_16x16x32_bf16 v[54:57], v[166:169], v[182:185], v[98:101]
	v_mfma_f32_16x16x32_bf16 v[98:101], v[170:173], v[198:201], v[54:57]
	v_mfma_f32_16x16x32_bf16 v[54:57], v[174:177], v[182:185], v[94:97]
	v_mfma_f32_16x16x32_bf16 v[94:97], v[178:181], v[198:201], v[54:57]
	s_setprio 0
	s_setprio 1
	v_mfma_f32_16x16x32_bf16 v[54:57], v[150:153], v[194:197], v[138:141]
	v_mfma_f32_16x16x32_bf16 v[138:141], v[154:157], v[210:213], v[54:57]
	v_mfma_f32_16x16x32_bf16 v[54:57], v[158:161], v[194:197], v[134:137]
	v_mfma_f32_16x16x32_bf16 v[134:137], v[162:165], v[210:213], v[54:57]
	s_setprio 0
	s_setprio 1
	v_mfma_f32_16x16x32_bf16 v[54:57], v[150:153], v[190:193], v[122:125]
	v_mfma_f32_16x16x32_bf16 v[122:125], v[154:157], v[206:209], v[54:57]
	v_mfma_f32_16x16x32_bf16 v[54:57], v[158:161], v[190:193], v[118:121]
	v_mfma_f32_16x16x32_bf16 v[118:121], v[162:165], v[206:209], v[54:57]
	s_setprio 0
	s_setprio 1
	v_mfma_f32_16x16x32_bf16 v[54:57], v[150:153], v[186:189], v[106:109]
	v_mfma_f32_16x16x32_bf16 v[106:109], v[154:157], v[202:205], v[54:57]
	v_mfma_f32_16x16x32_bf16 v[54:57], v[158:161], v[186:189], v[102:105]
	v_mfma_f32_16x16x32_bf16 v[102:105], v[162:165], v[202:205], v[54:57]
	s_setprio 0
	s_setprio 1
	v_mfma_f32_16x16x32_bf16 v[54:57], v[150:153], v[182:185], v[90:93]
	v_mfma_f32_16x16x32_bf16 v[90:93], v[154:157], v[198:201], v[54:57]
	v_mfma_f32_16x16x32_bf16 v[54:57], v[158:161], v[182:185], v[86:89]
	v_mfma_f32_16x16x32_bf16 v[86:89], v[162:165], v[198:201], v[54:57]
	s_setprio 0
	s_barrier
	s_and_b64 vcc, exec, s[0:1]
	s_cbranch_vccnz .LBB0_1562
	ds_read_b128 v[194:197], v248 offset:49152
	ds_read_b128 v[210:213], v248 offset:50176
	ds_read_b128 v[190:193], v248 offset:51200
	ds_read_b128 v[206:209], v248 offset:52224
	ds_read_b128 v[186:189], v248 offset:53248
	ds_read_b128 v[202:205], v248 offset:54272
	ds_read_b128 v[182:185], v248 offset:55296
	ds_read_b128 v[198:201], v248 offset:56320
.LBB0_1562:
	s_mov_b32 m0, s56
	s_nop 1
	v_lshl_add_u64 v[54:55], v[226:227], 0, s[66:67]
	s_add_u32 s42, s42, 0x40080
	global_load_lds_dwordx4 v[54:55], off
	v_lshl_add_u64 v[54:55], v[228:229], 0, s[66:67]
	s_mov_b32 m0, s57
	s_addc_u32 s43, s43, 0
	global_load_lds_dwordx4 v[54:55], off
	v_lshl_add_u64 v[54:55], s[42:43], 0, v[0:1]
	s_mov_b32 m0, s60
	s_and_b64 vcc, exec, s[0:1]
	global_load_lds_dwordx4 v[54:55], off
	v_lshl_add_u64 v[54:55], s[42:43], 0, v[220:221]
	s_mov_b32 m0, s61
	s_nop 0
	global_load_lds_dwordx4 v[54:55], off
	v_lshl_add_u64 v[54:55], v[230:231], 0, s[66:67]
	s_mov_b32 m0, s58
	s_nop 0
	global_load_lds_dwordx4 v[54:55], off
	v_lshl_add_u64 v[54:55], v[232:233], 0, s[66:67]
	s_mov_b32 m0, s59
	s_nop 0
	global_load_lds_dwordx4 v[54:55], off
	s_waitcnt vmcnt(8)
	s_waitcnt lgkmcnt(0)
	s_barrier
	s_cbranch_vccnz .LBB0_1555
	s_setprio 1
	s_waitcnt lgkmcnt(0)
	v_mfma_f32_16x16x32_bf16 v[54:57], v[166:169], v[194:197], v[82:85]
	v_mfma_f32_16x16x32_bf16 v[82:85], v[170:173], v[210:213], v[54:57]
	v_mfma_f32_16x16x32_bf16 v[54:57], v[174:177], v[194:197], v[78:81]
	v_mfma_f32_16x16x32_bf16 v[50:53], v[166:169], v[190:193], v[50:53]
	s_setprio 0
	s_setprio 1
	v_mfma_f32_16x16x32_bf16 v[46:49], v[174:177], v[190:193], v[46:49]
	v_mfma_f32_16x16x32_bf16 v[34:37], v[166:169], v[186:189], v[34:37]
	v_mfma_f32_16x16x32_bf16 v[30:33], v[174:177], v[186:189], v[30:33]
	v_mfma_f32_16x16x32_bf16 v[18:21], v[166:169], v[182:185], v[18:21]
	s_setprio 0
	s_setprio 1
	v_mfma_f32_16x16x32_bf16 v[14:17], v[174:177], v[182:185], v[14:17]
	v_mfma_f32_16x16x32_bf16 v[78:81], v[178:181], v[210:213], v[54:57]
	v_mfma_f32_16x16x32_bf16 v[50:53], v[170:173], v[206:209], v[50:53]
	v_mfma_f32_16x16x32_bf16 v[46:49], v[178:181], v[206:209], v[46:49]
	s_setprio 0
	s_setprio 1
	v_mfma_f32_16x16x32_bf16 v[34:37], v[170:173], v[202:205], v[34:37]
	v_mfma_f32_16x16x32_bf16 v[30:33], v[178:181], v[202:205], v[30:33]
	v_mfma_f32_16x16x32_bf16 v[18:21], v[170:173], v[198:201], v[18:21]
	v_mfma_f32_16x16x32_bf16 v[14:17], v[178:181], v[198:201], v[14:17]
	s_setprio 0
	s_setprio 1
	v_mfma_f32_16x16x32_bf16 v[54:57], v[150:153], v[194:197], v[70:73]
	v_mfma_f32_16x16x32_bf16 v[70:73], v[154:157], v[210:213], v[54:57]
	v_mfma_f32_16x16x32_bf16 v[54:57], v[158:161], v[194:197], v[62:65]
	v_mfma_f32_16x16x32_bf16 v[42:45], v[150:153], v[190:193], v[42:45]
	s_setprio 0
	s_setprio 1
	v_mfma_f32_16x16x32_bf16 v[38:41], v[158:161], v[190:193], v[38:41]
	v_mfma_f32_16x16x32_bf16 v[26:29], v[150:153], v[186:189], v[26:29]
	v_mfma_f32_16x16x32_bf16 v[22:25], v[158:161], v[186:189], v[22:25]
	v_mfma_f32_16x16x32_bf16 v[10:13], v[150:153], v[182:185], v[10:13]
	s_setprio 0
	s_setprio 1
	v_mfma_f32_16x16x32_bf16 v[6:9], v[158:161], v[182:185], v[6:9]
	v_mfma_f32_16x16x32_bf16 v[62:65], v[162:165], v[210:213], v[54:57]
	v_mfma_f32_16x16x32_bf16 v[42:45], v[154:157], v[206:209], v[42:45]
	v_mfma_f32_16x16x32_bf16 v[38:41], v[162:165], v[206:209], v[38:41]
	s_setprio 0
	s_setprio 1
	v_mfma_f32_16x16x32_bf16 v[26:29], v[154:157], v[202:205], v[26:29]
	v_mfma_f32_16x16x32_bf16 v[22:25], v[162:165], v[202:205], v[22:25]
	v_mfma_f32_16x16x32_bf16 v[10:13], v[154:157], v[198:201], v[10:13]
	v_mfma_f32_16x16x32_bf16 v[6:9], v[162:165], v[198:201], v[6:9]
	s_setprio 0
	s_branch .LBB0_1555

.Lrw_done_g1_0:
	s_waitcnt lgkmcnt(0)
	v_mov_b32_e32 v169, v1
	s_barrier
	s_setprio 1
	s_waitcnt lgkmcnt(0)
	v_mfma_scale_f32_16x16x128_f8f6f4 v[150:153], v[26:33], v[198:205], 0, v234, v235 op_sel_hi:[0,0,0]
	v_mfma_scale_f32_16x16x128_f8f6f4 v[146:149], v[18:25], v[198:205], 0, v234, v235 op_sel_hi:[0,0,0]
	s_setprio 0
	s_setprio 1
	v_mfma_scale_f32_16x16x128_f8f6f4 v[142:145], v[26:33], v[206:213], 0, v234, v235 op_sel_hi:[0,0,0]
	v_mfma_scale_f32_16x16x128_f8f6f4 v[138:141], v[18:25], v[206:213], 0, v234, v235 op_sel_hi:[0,0,0]
	s_setprio 0
	s_setprio 1
	v_mfma_scale_f32_16x16x128_f8f6f4 v[134:137], v[26:33], v[216:223], 0, v234, v235 op_sel_hi:[0,0,0]
	v_mfma_scale_f32_16x16x128_f8f6f4 v[130:133], v[18:25], v[216:223], 0, v234, v235 op_sel_hi:[0,0,0]
	s_setprio 0
	s_setprio 1
	v_mfma_scale_f32_16x16x128_f8f6f4 v[126:129], v[26:33], v[224:231], 0, v234, v235 op_sel_hi:[0,0,0]
	v_mfma_scale_f32_16x16x128_f8f6f4 v[122:125], v[18:25], v[224:231], 0, v234, v235 op_sel_hi:[0,0,0]
	s_setprio 0
	s_setprio 1
	v_mfma_scale_f32_16x16x128_f8f6f4 v[118:121], v[10:17], v[198:205], 0, v234, v235 op_sel_hi:[0,0,0]
	v_mfma_scale_f32_16x16x128_f8f6f4 v[114:117], v[2:9], v[198:205], 0, v234, v235 op_sel_hi:[0,0,0]
	s_setprio 0
	s_setprio 1
	v_mfma_scale_f32_16x16x128_f8f6f4 v[110:113], v[10:17], v[206:213], 0, v234, v235 op_sel_hi:[0,0,0]
	v_mfma_scale_f32_16x16x128_f8f6f4 v[106:109], v[2:9], v[206:213], 0, v234, v235 op_sel_hi:[0,0,0]
	s_setprio 0
	s_setprio 1
	v_mfma_scale_f32_16x16x128_f8f6f4 v[102:105], v[10:17], v[216:223], 0, v234, v235 op_sel_hi:[0,0,0]
	v_mfma_scale_f32_16x16x128_f8f6f4 v[98:101], v[2:9], v[216:223], 0, v234, v235 op_sel_hi:[0,0,0]
	s_setprio 0
	s_setprio 1
	v_mfma_scale_f32_16x16x128_f8f6f4 v[94:97], v[10:17], v[224:231], 0, v234, v235 op_sel_hi:[0,0,0]
	v_mfma_scale_f32_16x16x128_f8f6f4 v[90:93], v[2:9], v[224:231], 0, v234, v235 op_sel_hi:[0,0,0]
	s_setprio 0
	s_barrier
	v_lshl_add_u64 v[170:171], s[4:5], 0, v[162:163]
	s_mov_b64 s[54:55], 0x100
	s_mov_b32 m0, s68
	v_lshl_add_u64 v[172:173], v[170:171], 0, s[54:55]
	ds_read_b128 v[198:201], v192 offset:16384
	ds_read_b128 v[202:205], v192 offset:17408
	ds_read_b128 v[206:209], v192 offset:18432
	ds_read_b128 v[210:213], v192 offset:19456
	ds_read_b128 v[216:219], v192 offset:20480
	ds_read_b128 v[220:223], v192 offset:21504
	ds_read_b128 v[224:227], v192 offset:22528
	ds_read_b128 v[228:231], v192 offset:23552
	global_load_lds_dwordx4 v[172:173], off
	v_lshl_add_u64 v[172:173], s[4:5], 0, v[164:165]
	v_lshl_add_u64 v[232:233], v[172:173], 0, s[54:55]
	s_add_u32 s54, s4, 0x20100
	s_mov_b32 m0, s60
	s_addc_u32 s55, s5, 0
	global_load_lds_dwordx4 v[232:233], off
	v_lshl_add_u64 v[232:233], s[54:55], 0, v[162:163]
	s_mov_b32 m0, s61
	v_lshlrev_b32_e32 v0, 10, v195
	global_load_lds_dwordx4 v[232:233], off
	v_lshl_add_u64 v[232:233], s[54:55], 0, v[164:165]
	s_mov_b32 m0, s62
	v_and_or_b32 v0, v0, s82, v174
	global_load_lds_dwordx4 v[232:233], off
	v_bfe_u32 v197, v195, 16, 16
	s_mov_b32 m0, s65
	v_lshl_add_u32 v197, v197, 10, v175
	global_load_lds_dwordx4 v0, s[34:35]
	s_mov_b32 m0, s63
	s_nop 0
	global_load_lds_dwordx4 v197, s[34:35]
	s_cmp_eq_u32 s23, 0
	s_cbranch_scc1 .Lrw_first_g1_1
	s_waitcnt vmcnt(12)
	s_branch .Lrw_done_g1_1

.Lrw_done_g1_1:
	s_waitcnt lgkmcnt(0)
	s_barrier
	s_setprio 1
	s_waitcnt lgkmcnt(0)
	v_mfma_scale_f32_16x16x128_f8f6f4 v[86:89], v[26:33], v[198:205], 0, v234, v235 op_sel_hi:[0,0,0]
	v_mfma_scale_f32_16x16x128_f8f6f4 v[82:85], v[18:25], v[198:205], 0, v234, v235 op_sel_hi:[0,0,0]
	s_setprio 0
	s_setprio 1
	v_mfma_scale_f32_16x16x128_f8f6f4 v[78:81], v[26:33], v[206:213], 0, v234, v235 op_sel_hi:[0,0,0]
	v_mfma_scale_f32_16x16x128_f8f6f4 v[74:77], v[18:25], v[206:213], 0, v234, v235 op_sel_hi:[0,0,0]
	s_setprio 0
	s_setprio 1
	v_mfma_scale_f32_16x16x128_f8f6f4 v[70:73], v[26:33], v[216:223], 0, v234, v235 op_sel_hi:[0,0,0]
	v_mfma_scale_f32_16x16x128_f8f6f4 v[66:69], v[18:25], v[216:223], 0, v234, v235 op_sel_hi:[0,0,0]
	s_setprio 0
	s_setprio 1
	v_mfma_scale_f32_16x16x128_f8f6f4 v[62:65], v[26:33], v[224:231], 0, v234, v235 op_sel_hi:[0,0,0]
	v_mfma_scale_f32_16x16x128_f8f6f4 v[58:61], v[18:25], v[224:231], 0, v234, v235 op_sel_hi:[0,0,0]
	s_setprio 0
	s_setprio 1
	v_mfma_scale_f32_16x16x128_f8f6f4 v[54:57], v[10:17], v[198:205], 0, v234, v235 op_sel_hi:[0,0,0]
	v_mfma_scale_f32_16x16x128_f8f6f4 v[50:53], v[2:9], v[198:205], 0, v234, v235 op_sel_hi:[0,0,0]
	s_setprio 0
	s_setprio 1
	v_mfma_scale_f32_16x16x128_f8f6f4 v[46:49], v[10:17], v[206:213], 0, v234, v235 op_sel_hi:[0,0,0]
	v_mfma_scale_f32_16x16x128_f8f6f4 v[42:45], v[2:9], v[206:213], 0, v234, v235 op_sel_hi:[0,0,0]
	s_setprio 0
	s_setprio 1
	v_mfma_scale_f32_16x16x128_f8f6f4 v[38:41], v[10:17], v[216:223], 0, v234, v235 op_sel_hi:[0,0,0]
	v_mfma_scale_f32_16x16x128_f8f6f4 v[34:37], v[2:9], v[216:223], 0, v234, v235 op_sel_hi:[0,0,0]
	s_setprio 0
	s_setprio 1
	v_mfma_scale_f32_16x16x128_f8f6f4 v[154:157], v[10:17], v[224:231], 0, v234, v235 op_sel_hi:[0,0,0]
	v_mfma_scale_f32_16x16x128_f8f6f4 v[158:161], v[2:9], v[224:231], 0, v234, v235 op_sel_hi:[0,0,0]
	s_setprio 0
	s_barrier
	ds_read_b128 v[18:21], v184
	ds_read_b128 v[22:25], v185
	ds_read_b128 v[26:29], v186
	ds_read_b128 v[30:33], v187
	ds_read_b128 v[2:5], v188
	ds_read_b128 v[6:9], v189
	ds_read_b128 v[10:13], v190
	ds_read_b128 v[14:17], v191
	s_mov_b32 m0, s10
	ds_read_b128 v[198:201], v192 offset:32768
	ds_read_b128 v[202:205], v192 offset:33792
	ds_read_b128 v[206:209], v192 offset:34816
	ds_read_b128 v[210:213], v192 offset:35840
	ds_read_b128 v[216:219], v192 offset:36864
	ds_read_b128 v[220:223], v192 offset:37888
	ds_read_b128 v[224:227], v192 offset:38912
	ds_read_b128 v[228:231], v192 offset:39936
	global_load_lds_dwordx4 v166, s[34:35]
	s_mov_b32 m0, s11
	s_nop 0
	global_load_lds_dwordx4 v168, s[34:35]
	s_waitcnt vmcnt(8)
	s_waitcnt lgkmcnt(0)
	s_barrier
	s_setprio 1
	s_waitcnt lgkmcnt(0)
	v_mfma_scale_f32_16x16x128_f8f6f4 v[150:153], v[18:25], v[198:205], v[150:153], v234, v235 op_sel_hi:[0,0,0]
	v_mfma_scale_f32_16x16x128_f8f6f4 v[146:149], v[26:33], v[198:205], v[146:149], v234, v235 op_sel_hi:[0,0,0]
	s_setprio 0
	s_setprio 1
	v_mfma_scale_f32_16x16x128_f8f6f4 v[142:145], v[18:25], v[206:213], v[142:145], v234, v235 op_sel_hi:[0,0,0]
	v_mfma_scale_f32_16x16x128_f8f6f4 v[138:141], v[26:33], v[206:213], v[138:141], v234, v235 op_sel_hi:[0,0,0]
	s_setprio 0
	s_setprio 1
	v_mfma_scale_f32_16x16x128_f8f6f4 v[134:137], v[18:25], v[216:223], v[134:137], v234, v235 op_sel_hi:[0,0,0]
	v_mfma_scale_f32_16x16x128_f8f6f4 v[130:133], v[26:33], v[216:223], v[130:133], v234, v235 op_sel_hi:[0,0,0]
	s_setprio 0
	s_setprio 1
	v_mfma_scale_f32_16x16x128_f8f6f4 v[126:129], v[18:25], v[224:231], v[126:129], v234, v235 op_sel_hi:[0,0,0]
	v_mfma_scale_f32_16x16x128_f8f6f4 v[122:125], v[26:33], v[224:231], v[122:125], v234, v235 op_sel_hi:[0,0,0]
	s_setprio 0
	s_setprio 1
	v_mfma_scale_f32_16x16x128_f8f6f4 v[118:121], v[2:9], v[198:205], v[118:121], v234, v235 op_sel_hi:[0,0,0]
	v_mfma_scale_f32_16x16x128_f8f6f4 v[114:117], v[10:17], v[198:205], v[114:117], v234, v235 op_sel_hi:[0,0,0]
	s_setprio 0
	s_setprio 1
	v_mfma_scale_f32_16x16x128_f8f6f4 v[110:113], v[2:9], v[206:213], v[110:113], v234, v235 op_sel_hi:[0,0,0]
	v_mfma_scale_f32_16x16x128_f8f6f4 v[106:109], v[10:17], v[206:213], v[106:109], v234, v235 op_sel_hi:[0,0,0]
	s_setprio 0
	s_setprio 1
	v_mfma_scale_f32_16x16x128_f8f6f4 v[102:105], v[2:9], v[216:223], v[102:105], v234, v235 op_sel_hi:[0,0,0]
	v_mfma_scale_f32_16x16x128_f8f6f4 v[98:101], v[10:17], v[216:223], v[98:101], v234, v235 op_sel_hi:[0,0,0]
	s_setprio 0
	s_setprio 1
	v_mfma_scale_f32_16x16x128_f8f6f4 v[94:97], v[2:9], v[224:231], v[94:97], v234, v235 op_sel_hi:[0,0,0]
	v_mfma_scale_f32_16x16x128_f8f6f4 v[90:93], v[10:17], v[224:231], v[90:93], v234, v235 op_sel_hi:[0,0,0]
	s_setprio 0
	s_barrier
	s_mov_b64 s[54:55], 0x180
	s_mov_b32 m0, s64
	v_lshl_add_u64 v[170:171], v[170:171], 0, s[54:55]
	ds_read_b128 v[198:201], v192 offset:49152
	ds_read_b128 v[202:205], v192 offset:50176
	ds_read_b128 v[206:209], v192 offset:51200
	ds_read_b128 v[210:213], v192 offset:52224
	ds_read_b128 v[216:219], v192 offset:53248
	ds_read_b128 v[220:223], v192 offset:54272
	ds_read_b128 v[224:227], v192 offset:55296
	ds_read_b128 v[228:231], v192 offset:56320
	global_load_lds_dwordx4 v[170:171], off
	v_lshl_add_u64 v[170:171], v[172:173], 0, s[54:55]
	s_add_u32 s54, s4, 0x20180
	s_mov_b32 m0, s81
	s_addc_u32 s55, s5, 0
	global_load_lds_dwordx4 v[170:171], off
	v_lshl_add_u64 v[170:171], s[54:55], 0, v[162:163]
	s_mov_b32 m0, s49
	s_nop 0
	global_load_lds_dwordx4 v[170:171], off
	v_lshl_add_u64 v[170:171], s[54:55], 0, v[164:165]
	s_mov_b32 m0, s30
	s_nop 0
	global_load_lds_dwordx4 v[170:171], off
	s_mov_b32 m0, s6
	s_nop 0
	global_load_lds_dwordx4 v0, s[36:37]
	s_mov_b32 m0, s7
	s_nop 0
	global_load_lds_dwordx4 v197, s[36:37]
	s_waitcnt vmcnt(8)
	s_waitcnt lgkmcnt(0)
	s_barrier
	s_setprio 1
	s_waitcnt lgkmcnt(0)
	v_mfma_scale_f32_16x16x128_f8f6f4 v[86:89], v[18:25], v[198:205], v[86:89], v234, v235 op_sel_hi:[0,0,0]
	v_mfma_scale_f32_16x16x128_f8f6f4 v[82:85], v[26:33], v[198:205], v[82:85], v234, v235 op_sel_hi:[0,0,0]
	s_setprio 0
	s_setprio 1
	v_mfma_scale_f32_16x16x128_f8f6f4 v[78:81], v[18:25], v[206:213], v[78:81], v234, v235 op_sel_hi:[0,0,0]
	v_mfma_scale_f32_16x16x128_f8f6f4 v[74:77], v[26:33], v[206:213], v[74:77], v234, v235 op_sel_hi:[0,0,0]
	s_setprio 0
	s_setprio 1
	v_mfma_scale_f32_16x16x128_f8f6f4 v[70:73], v[18:25], v[216:223], v[70:73], v234, v235 op_sel_hi:[0,0,0]
	v_mfma_scale_f32_16x16x128_f8f6f4 v[66:69], v[26:33], v[216:223], v[66:69], v234, v235 op_sel_hi:[0,0,0]
	s_setprio 0
	s_setprio 1
	v_mfma_scale_f32_16x16x128_f8f6f4 v[62:65], v[18:25], v[224:231], v[62:65], v234, v235 op_sel_hi:[0,0,0]
	v_mfma_scale_f32_16x16x128_f8f6f4 v[58:61], v[26:33], v[224:231], v[58:61], v234, v235 op_sel_hi:[0,0,0]
	s_setprio 0
	s_setprio 1
	v_mfma_scale_f32_16x16x128_f8f6f4 v[54:57], v[2:9], v[198:205], v[54:57], v234, v235 op_sel_hi:[0,0,0]
	v_mfma_scale_f32_16x16x128_f8f6f4 v[50:53], v[10:17], v[198:205], v[50:53], v234, v235 op_sel_hi:[0,0,0]
	s_setprio 0
	s_setprio 1
	v_mfma_scale_f32_16x16x128_f8f6f4 v[46:49], v[2:9], v[206:213], v[46:49], v234, v235 op_sel_hi:[0,0,0]
	v_mfma_scale_f32_16x16x128_f8f6f4 v[42:45], v[10:17], v[206:213], v[42:45], v234, v235 op_sel_hi:[0,0,0]
	s_setprio 0
	s_setprio 1
	v_mfma_scale_f32_16x16x128_f8f6f4 v[38:41], v[2:9], v[216:223], v[38:41], v234, v235 op_sel_hi:[0,0,0]
	v_mfma_scale_f32_16x16x128_f8f6f4 v[34:37], v[10:17], v[216:223], v[34:37], v234, v235 op_sel_hi:[0,0,0]
	s_setprio 0
	s_setprio 1
	v_mfma_scale_f32_16x16x128_f8f6f4 v[154:157], v[2:9], v[224:231], v[154:157], v234, v235 op_sel_hi:[0,0,0]
	v_mfma_scale_f32_16x16x128_f8f6f4 v[158:161], v[10:17], v[224:231], v[158:161], v234, v235 op_sel_hi:[0,0,0]
	s_setprio 0
	s_barrier
	s_add_u32 s43, s4, 0x200
	s_addc_u32 s45, s5, 0
	s_mov_b32 s74, 0
	s_mov_b64 s[54:55], s[36:37]
	s_branch .LBB0_2003
.LBB0_2002:
	ds_read_b128 v[2:5], v183
	ds_read_b128 v[6:9], v182
	ds_read_b128 v[10:13], v181
	ds_read_b128 v[14:17], v180
	ds_read_b128 v[26:29], v179
	ds_read_b128 v[30:33], v178
	ds_read_b128 v[198:201], v177
	ds_read_b128 v[202:205], v176
	s_add_u32 s58, s54, 0x80
	s_addc_u32 s59, s55, 0
	s_and_b64 s[56:57], s[4:5], exec
	s_cselect_b32 s59, s9, s59
	s_cselect_b32 s58, s8, s58
	s_cselect_b32 s57, s47, s45
	s_cselect_b32 s56, s46, s43
	s_mov_b32 m0, s27
	v_lshl_add_u64 v[170:171], s[54:55], 0, v[166:167]
	ds_read_b128 v[18:21], v192
	ds_read_b128 v[22:25], v192 offset:1024
	ds_read_b128 v[206:209], v192 offset:2048
	ds_read_b128 v[210:213], v192 offset:3072
	ds_read_b128 v[216:219], v192 offset:4096
	ds_read_b128 v[220:223], v192 offset:5120
	ds_read_b128 v[224:227], v192 offset:6144
	ds_read_b128 v[228:231], v192 offset:7168
	global_load_lds_dwordx4 v[170:171], off
	v_lshl_add_u64 v[170:171], s[54:55], 0, v[168:169]
	s_mov_b32 m0, s41
	s_nop 0
	global_load_lds_dwordx4 v[170:171], off
	s_waitcnt vmcnt(8)
	s_waitcnt lgkmcnt(0)
	s_barrier
	s_setprio 1
	s_waitcnt lgkmcnt(0)
	v_mfma_scale_f32_16x16x128_f8f6f4 v[150:153], v[2:9], v[18:25], v[150:153], v234, v235 op_sel_hi:[0,0,0]
	v_mfma_scale_f32_16x16x128_f8f6f4 v[146:149], v[10:17], v[18:25], v[146:149], v234, v235 op_sel_hi:[0,0,0]
	s_setprio 0
	s_setprio 1
	v_mfma_scale_f32_16x16x128_f8f6f4 v[142:145], v[2:9], v[206:213], v[142:145], v234, v235 op_sel_hi:[0,0,0]
	v_mfma_scale_f32_16x16x128_f8f6f4 v[138:141], v[10:17], v[206:213], v[138:141], v234, v235 op_sel_hi:[0,0,0]
	s_setprio 0
	s_setprio 1
	v_mfma_scale_f32_16x16x128_f8f6f4 v[134:137], v[2:9], v[216:223], v[134:137], v234, v235 op_sel_hi:[0,0,0]
	v_mfma_scale_f32_16x16x128_f8f6f4 v[130:133], v[10:17], v[216:223], v[130:133], v234, v235 op_sel_hi:[0,0,0]
	s_setprio 0
	s_setprio 1
	v_mfma_scale_f32_16x16x128_f8f6f4 v[126:129], v[2:9], v[224:231], v[126:129], v234, v235 op_sel_hi:[0,0,0]
	v_mfma_scale_f32_16x16x128_f8f6f4 v[122:125], v[10:17], v[224:231], v[122:125], v234, v235 op_sel_hi:[0,0,0]
	s_setprio 0
	s_setprio 1
	v_mfma_scale_f32_16x16x128_f8f6f4 v[118:121], v[26:33], v[18:25], v[118:121], v234, v235 op_sel_hi:[0,0,0]
	v_mfma_scale_f32_16x16x128_f8f6f4 v[114:117], v[198:205], v[18:25], v[114:117], v234, v235 op_sel_hi:[0,0,0]
	s_setprio 0
	s_setprio 1
	v_mfma_scale_f32_16x16x128_f8f6f4 v[110:113], v[26:33], v[206:213], v[110:113], v234, v235 op_sel_hi:[0,0,0]
	v_mfma_scale_f32_16x16x128_f8f6f4 v[106:109], v[198:205], v[206:213], v[106:109], v234, v235 op_sel_hi:[0,0,0]
	s_setprio 0
	s_setprio 1
	v_mfma_scale_f32_16x16x128_f8f6f4 v[102:105], v[26:33], v[216:223], v[102:105], v234, v235 op_sel_hi:[0,0,0]
	v_mfma_scale_f32_16x16x128_f8f6f4 v[98:101], v[198:205], v[216:223], v[98:101], v234, v235 op_sel_hi:[0,0,0]
	s_setprio 0
	s_setprio 1
	v_mfma_scale_f32_16x16x128_f8f6f4 v[94:97], v[26:33], v[224:231], v[94:97], v234, v235 op_sel_hi:[0,0,0]
	v_mfma_scale_f32_16x16x128_f8f6f4 v[90:93], v[198:205], v[224:231], v[90:93], v234, v235 op_sel_hi:[0,0,0]
	s_setprio 0
	s_barrier
	s_mov_b32 m0, s68
	v_lshl_add_u64 v[18:19], s[56:57], 0, v[162:163]
	s_add_u32 vcc_lo, s56, 0x20000
	ds_read_b128 v[206:209], v192 offset:16384
	ds_read_b128 v[210:213], v192 offset:17408
	ds_read_b128 v[216:219], v192 offset:18432
	ds_read_b128 v[220:223], v192 offset:19456
	ds_read_b128 v[224:227], v192 offset:20480
	ds_read_b128 v[228:231], v192 offset:21504
	ds_read_b128 v[244:247], v192 offset:22528
	ds_read_b128 v[248:251], v192 offset:23552
	global_load_lds_dwordx4 v[18:19], off
	v_lshl_add_u64 v[20:21], s[56:57], 0, v[164:165]
	s_mov_b32 m0, s60
	s_addc_u32 vcc_hi, s57, 0
	global_load_lds_dwordx4 v[20:21], off
	v_lshl_add_u64 v[22:23], vcc, 0, v[162:163]
	s_mov_b32 m0, s61
	s_nop 0
	global_load_lds_dwordx4 v[22:23], off
	v_lshl_add_u64 v[22:23], vcc, 0, v[164:165]
	s_mov_b32 m0, s62
	s_nop 0
	global_load_lds_dwordx4 v[22:23], off
	v_cndmask_b32_e64 v22, v195, v193, s[4:5]
	v_lshlrev_b32_e32 v0, 10, v22
	v_and_or_b32 v0, v0, s82, v174
	v_bfe_u32 v22, v22, 16, 16
	s_mov_b32 m0, s65
	v_lshl_add_u32 v22, v22, 10, v175
	global_load_lds_dwordx4 v0, s[58:59]
	s_mov_b32 m0, s63
	v_mov_b32_e32 v23, v1
	global_load_lds_dwordx4 v22, s[58:59]
	s_waitcnt vmcnt(8)
	s_waitcnt lgkmcnt(0)
	v_lshl_add_u64 v[24:25], s[58:59], 0, v[0:1]
	v_lshl_add_u64 v[22:23], s[58:59], 0, v[22:23]
	s_barrier
	s_setprio 1
	s_waitcnt lgkmcnt(0)
	v_mfma_scale_f32_16x16x128_f8f6f4 v[86:89], v[2:9], v[206:213], v[86:89], v234, v235 op_sel_hi:[0,0,0]
	v_mfma_scale_f32_16x16x128_f8f6f4 v[82:85], v[10:17], v[206:213], v[82:85], v234, v235 op_sel_hi:[0,0,0]
	s_setprio 0
	s_setprio 1
	v_mfma_scale_f32_16x16x128_f8f6f4 v[78:81], v[2:9], v[216:223], v[78:81], v234, v235 op_sel_hi:[0,0,0]
	v_mfma_scale_f32_16x16x128_f8f6f4 v[74:77], v[10:17], v[216:223], v[74:77], v234, v235 op_sel_hi:[0,0,0]
	s_setprio 0
	s_setprio 1
	v_mfma_scale_f32_16x16x128_f8f6f4 v[70:73], v[2:9], v[224:231], v[70:73], v234, v235 op_sel_hi:[0,0,0]
	v_mfma_scale_f32_16x16x128_f8f6f4 v[66:69], v[10:17], v[224:231], v[66:69], v234, v235 op_sel_hi:[0,0,0]
	s_setprio 0
	s_setprio 1
	v_mfma_scale_f32_16x16x128_f8f6f4 v[62:65], v[2:9], v[244:251], v[62:65], v234, v235 op_sel_hi:[0,0,0]
	v_mfma_scale_f32_16x16x128_f8f6f4 v[58:61], v[10:17], v[244:251], v[58:61], v234, v235 op_sel_hi:[0,0,0]
	s_setprio 0
	s_setprio 1
	v_mfma_scale_f32_16x16x128_f8f6f4 v[54:57], v[26:33], v[206:213], v[54:57], v234, v235 op_sel_hi:[0,0,0]
	v_mfma_scale_f32_16x16x128_f8f6f4 v[50:53], v[198:205], v[206:213], v[50:53], v234, v235 op_sel_hi:[0,0,0]
	s_setprio 0
	s_setprio 1
	v_mfma_scale_f32_16x16x128_f8f6f4 v[46:49], v[26:33], v[216:223], v[46:49], v234, v235 op_sel_hi:[0,0,0]
	v_mfma_scale_f32_16x16x128_f8f6f4 v[42:45], v[198:205], v[216:223], v[42:45], v234, v235 op_sel_hi:[0,0,0]
	s_setprio 0
	s_setprio 1
	v_mfma_scale_f32_16x16x128_f8f6f4 v[38:41], v[26:33], v[224:231], v[38:41], v234, v235 op_sel_hi:[0,0,0]
	v_mfma_scale_f32_16x16x128_f8f6f4 v[34:37], v[198:205], v[224:231], v[34:37], v234, v235 op_sel_hi:[0,0,0]
	s_setprio 0
	s_setprio 1
	v_mfma_scale_f32_16x16x128_f8f6f4 v[154:157], v[26:33], v[244:251], v[154:157], v234, v235 op_sel_hi:[0,0,0]
	v_mfma_scale_f32_16x16x128_f8f6f4 v[158:161], v[198:205], v[244:251], v[158:161], v234, v235 op_sel_hi:[0,0,0]
	s_setprio 0
	s_barrier
	ds_read_b128 v[10:13], v184
	ds_read_b128 v[14:17], v185
	ds_read_b128 v[26:29], v186
	ds_read_b128 v[30:33], v187
	ds_read_b128 v[2:5], v188
	ds_read_b128 v[6:9], v189
	ds_read_b128 v[198:201], v190
	ds_read_b128 v[202:205], v191
	v_cndmask_b32_e64 v0, v196, v194, s[4:5]
	v_lshlrev_b32_e32 v170, 10, v0
	s_mov_b32 m0, s10
	v_and_or_b32 v170, v170, s82, v174
	v_bfe_u32 v0, v0, 16, 16
	ds_read_b128 v[206:209], v192 offset:32768
	ds_read_b128 v[210:213], v192 offset:33792
	ds_read_b128 v[216:219], v192 offset:34816
	ds_read_b128 v[220:223], v192 offset:35840
	ds_read_b128 v[224:227], v192 offset:36864
	ds_read_b128 v[228:231], v192 offset:37888
	ds_read_b128 v[244:247], v192 offset:38912
	ds_read_b128 v[248:251], v192 offset:39936
	v_lshl_add_u32 v0, v0, 10, v175
	global_load_lds_dwordx4 v170, s[58:59]
	s_mov_b32 m0, s11
	s_nop 0
	global_load_lds_dwordx4 v0, s[58:59]
	s_waitcnt vmcnt(8)
	s_waitcnt lgkmcnt(0)
	s_barrier
	s_setprio 1
	s_waitcnt lgkmcnt(0)
	v_mfma_scale_f32_16x16x128_f8f6f4 v[150:153], v[10:17], v[206:213], v[150:153], v234, v235 op_sel_hi:[0,0,0]
	v_mfma_scale_f32_16x16x128_f8f6f4 v[146:149], v[26:33], v[206:213], v[146:149], v234, v235 op_sel_hi:[0,0,0]
	s_setprio 0
	s_setprio 1
	v_mfma_scale_f32_16x16x128_f8f6f4 v[142:145], v[10:17], v[216:223], v[142:145], v234, v235 op_sel_hi:[0,0,0]
	v_mfma_scale_f32_16x16x128_f8f6f4 v[138:141], v[26:33], v[216:223], v[138:141], v234, v235 op_sel_hi:[0,0,0]
	s_setprio 0
	s_setprio 1
	v_mfma_scale_f32_16x16x128_f8f6f4 v[134:137], v[10:17], v[224:231], v[134:137], v234, v235 op_sel_hi:[0,0,0]
	v_mfma_scale_f32_16x16x128_f8f6f4 v[130:133], v[26:33], v[224:231], v[130:133], v234, v235 op_sel_hi:[0,0,0]
	s_setprio 0
	s_setprio 1
	v_mfma_scale_f32_16x16x128_f8f6f4 v[126:129], v[10:17], v[244:251], v[126:129], v234, v235 op_sel_hi:[0,0,0]
	v_mfma_scale_f32_16x16x128_f8f6f4 v[122:125], v[26:33], v[244:251], v[122:125], v234, v235 op_sel_hi:[0,0,0]
	s_setprio 0
	s_setprio 1
	v_mfma_scale_f32_16x16x128_f8f6f4 v[118:121], v[2:9], v[206:213], v[118:121], v234, v235 op_sel_hi:[0,0,0]
	v_mfma_scale_f32_16x16x128_f8f6f4 v[114:117], v[198:205], v[206:213], v[114:117], v234, v235 op_sel_hi:[0,0,0]
	s_setprio 0
	s_setprio 1
	v_mfma_scale_f32_16x16x128_f8f6f4 v[110:113], v[2:9], v[216:223], v[110:113], v234, v235 op_sel_hi:[0,0,0]
	v_mfma_scale_f32_16x16x128_f8f6f4 v[106:109], v[198:205], v[216:223], v[106:109], v234, v235 op_sel_hi:[0,0,0]
	s_setprio 0
	s_setprio 1
	v_mfma_scale_f32_16x16x128_f8f6f4 v[102:105], v[2:9], v[224:231], v[102:105], v234, v235 op_sel_hi:[0,0,0]
	v_mfma_scale_f32_16x16x128_f8f6f4 v[98:101], v[198:205], v[224:231], v[98:101], v234, v235 op_sel_hi:[0,0,0]
	s_setprio 0
	s_setprio 1
	v_mfma_scale_f32_16x16x128_f8f6f4 v[94:97], v[2:9], v[244:251], v[94:97], v234, v235 op_sel_hi:[0,0,0]
	v_mfma_scale_f32_16x16x128_f8f6f4 v[90:93], v[198:205], v[244:251], v[90:93], v234, v235 op_sel_hi:[0,0,0]
	s_setprio 0
	s_barrier
	s_mov_b32 m0, s64
	v_lshl_add_u64 v[18:19], v[18:19], 0, s[66:67]
	s_add_u32 s4, s56, 0x20080
	ds_read_b128 v[206:209], v192 offset:49152
	ds_read_b128 v[210:213], v192 offset:50176
	ds_read_b128 v[216:219], v192 offset:51200
	ds_read_b128 v[220:223], v192 offset:52224
	ds_read_b128 v[224:227], v192 offset:53248
	ds_read_b128 v[228:231], v192 offset:54272
	ds_read_b128 v[244:247], v192 offset:55296
	ds_read_b128 v[248:251], v192 offset:56320
	global_load_lds_dwordx4 v[18:19], off
	v_lshl_add_u64 v[18:19], v[20:21], 0, s[66:67]
	s_mov_b32 m0, s81
	s_addc_u32 s5, s57, 0
	global_load_lds_dwordx4 v[18:19], off
	v_lshl_add_u64 v[18:19], s[4:5], 0, v[162:163]
	s_mov_b32 m0, s49
	s_nop 0
	global_load_lds_dwordx4 v[18:19], off
	v_lshl_add_u64 v[18:19], s[4:5], 0, v[164:165]
	s_mov_b32 m0, s30
	s_nop 0
	global_load_lds_dwordx4 v[18:19], off
	v_lshl_add_u64 v[18:19], v[24:25], 0, s[66:67]
	s_mov_b32 m0, s6
	s_nop 0
	global_load_lds_dwordx4 v[18:19], off
	v_lshl_add_u64 v[18:19], v[22:23], 0, s[66:67]
	s_mov_b32 m0, s7
	s_nop 0
	global_load_lds_dwordx4 v[18:19], off
	s_waitcnt vmcnt(8)
	s_waitcnt lgkmcnt(0)
	s_barrier
	s_setprio 1
	s_waitcnt lgkmcnt(0)
	v_mfma_scale_f32_16x16x128_f8f6f4 v[86:89], v[10:17], v[206:213], v[86:89], v234, v235 op_sel_hi:[0,0,0]
	v_mfma_scale_f32_16x16x128_f8f6f4 v[82:85], v[26:33], v[206:213], v[82:85], v234, v235 op_sel_hi:[0,0,0]
	s_setprio 0
	s_setprio 1
	v_mfma_scale_f32_16x16x128_f8f6f4 v[78:81], v[10:17], v[216:223], v[78:81], v234, v235 op_sel_hi:[0,0,0]
	v_mfma_scale_f32_16x16x128_f8f6f4 v[74:77], v[26:33], v[216:223], v[74:77], v234, v235 op_sel_hi:[0,0,0]
	s_setprio 0
	s_setprio 1
	v_mfma_scale_f32_16x16x128_f8f6f4 v[70:73], v[10:17], v[224:231], v[70:73], v234, v235 op_sel_hi:[0,0,0]
	v_mfma_scale_f32_16x16x128_f8f6f4 v[66:69], v[26:33], v[224:231], v[66:69], v234, v235 op_sel_hi:[0,0,0]
	s_setprio 0
	s_setprio 1
	v_mfma_scale_f32_16x16x128_f8f6f4 v[62:65], v[10:17], v[244:251], v[62:65], v234, v235 op_sel_hi:[0,0,0]
	v_mfma_scale_f32_16x16x128_f8f6f4 v[58:61], v[26:33], v[244:251], v[58:61], v234, v235 op_sel_hi:[0,0,0]
	s_setprio 0
	s_setprio 1
	v_mfma_scale_f32_16x16x128_f8f6f4 v[54:57], v[2:9], v[206:213], v[54:57], v234, v235 op_sel_hi:[0,0,0]
	v_mfma_scale_f32_16x16x128_f8f6f4 v[50:53], v[198:205], v[206:213], v[50:53], v234, v235 op_sel_hi:[0,0,0]
	s_setprio 0
	s_setprio 1
	v_mfma_scale_f32_16x16x128_f8f6f4 v[46:49], v[2:9], v[216:223], v[46:49], v234, v235 op_sel_hi:[0,0,0]
	v_mfma_scale_f32_16x16x128_f8f6f4 v[42:45], v[198:205], v[216:223], v[42:45], v234, v235 op_sel_hi:[0,0,0]
	s_setprio 0
	s_setprio 1
	v_mfma_scale_f32_16x16x128_f8f6f4 v[38:41], v[2:9], v[224:231], v[38:41], v234, v235 op_sel_hi:[0,0,0]
	v_mfma_scale_f32_16x16x128_f8f6f4 v[34:37], v[198:205], v[224:231], v[34:37], v234, v235 op_sel_hi:[0,0,0]
	s_setprio 0
	s_setprio 1
	v_mfma_scale_f32_16x16x128_f8f6f4 v[154:157], v[2:9], v[244:251], v[154:157], v234, v235 op_sel_hi:[0,0,0]
	v_mfma_scale_f32_16x16x128_f8f6f4 v[158:161], v[198:205], v[244:251], v[158:161], v234, v235 op_sel_hi:[0,0,0]
	s_setprio 0
	s_barrier
	s_add_i32 s74, s74, 2
	s_add_u32 s54, s54, 0x100
	s_addc_u32 s55, s55, 0
	s_add_u32 s43, s43, 0x100
	s_addc_u32 s45, s45, 0
	s_cmp_gt_u32 s74, 5
	s_cbranch_scc1 .LBB0_2005

.Lrw_done_g2_0:
	s_waitcnt lgkmcnt(0)
	s_barrier
	s_setprio 1
	s_waitcnt lgkmcnt(0)
	v_mfma_scale_f32_16x16x128_f8f6f4 v[158:161], v[18:25], v[172:179], 0, v234, v238 op_sel_hi:[0,0,0]
	v_mfma_scale_f32_16x16x128_f8f6f4 v[154:157], v[26:33], v[172:179], 0, v234, v238 op_sel_hi:[0,0,0]
	s_setprio 0
	s_setprio 1
	v_mfma_scale_f32_16x16x128_f8f6f4 v[150:153], v[18:25], v[198:205], 0, v234, v238 op_sel_hi:[0,0,0]
	v_mfma_scale_f32_16x16x128_f8f6f4 v[146:149], v[26:33], v[198:205], 0, v234, v238 op_sel_hi:[0,0,0]
	s_setprio 0
	s_setprio 1
	v_mfma_scale_f32_16x16x128_f8f6f4 v[142:145], v[18:25], v[206:213], 0, v234, v238 op_sel_hi:[0,0,0]
	v_mfma_scale_f32_16x16x128_f8f6f4 v[138:141], v[26:33], v[206:213], 0, v234, v238 op_sel_hi:[0,0,0]
	s_setprio 0
	s_setprio 1
	v_mfma_scale_f32_16x16x128_f8f6f4 v[134:137], v[18:25], v[216:223], 0, v234, v238 op_sel_hi:[0,0,0]
	v_mfma_scale_f32_16x16x128_f8f6f4 v[130:133], v[26:33], v[216:223], 0, v234, v238 op_sel_hi:[0,0,0]
	s_setprio 0
	s_setprio 1
	v_mfma_scale_f32_16x16x128_f8f6f4 v[126:129], v[2:9], v[172:179], 0, v234, v238 op_sel_hi:[0,0,0]
	v_mfma_scale_f32_16x16x128_f8f6f4 v[122:125], v[10:17], v[172:179], 0, v234, v238 op_sel_hi:[0,0,0]
	s_setprio 0
	s_setprio 1
	v_mfma_scale_f32_16x16x128_f8f6f4 v[118:121], v[2:9], v[198:205], 0, v234, v238 op_sel_hi:[0,0,0]
	v_mfma_scale_f32_16x16x128_f8f6f4 v[114:117], v[10:17], v[198:205], 0, v234, v238 op_sel_hi:[0,0,0]
	s_setprio 0
	s_setprio 1
	v_mfma_scale_f32_16x16x128_f8f6f4 v[110:113], v[2:9], v[206:213], 0, v234, v238 op_sel_hi:[0,0,0]
	v_mfma_scale_f32_16x16x128_f8f6f4 v[106:109], v[10:17], v[206:213], 0, v234, v238 op_sel_hi:[0,0,0]
	s_setprio 0
	s_setprio 1
	v_mfma_scale_f32_16x16x128_f8f6f4 v[102:105], v[2:9], v[216:223], 0, v234, v238 op_sel_hi:[0,0,0]
	v_mfma_scale_f32_16x16x128_f8f6f4 v[98:101], v[10:17], v[216:223], 0, v234, v238 op_sel_hi:[0,0,0]
	s_setprio 0
	s_barrier
	v_lshl_add_u64 v[172:173], s[44:45], 0, v[0:1]
	s_mov_b64 s[48:49], 0x100
	s_mov_b32 m0, s41
	v_lshl_add_u64 v[174:175], v[172:173], 0, s[48:49]
	ds_read_b128 v[198:201], v196 offset:16384
	ds_read_b128 v[202:205], v196 offset:17408
	ds_read_b128 v[206:209], v196 offset:18432
	ds_read_b128 v[210:213], v196 offset:19456
	ds_read_b128 v[216:219], v196 offset:20480
	ds_read_b128 v[220:223], v196 offset:21504
	ds_read_b128 v[224:227], v196 offset:22528
	ds_read_b128 v[228:231], v196 offset:23552
	global_load_lds_dwordx4 v[174:175], off
	v_lshl_add_u64 v[174:175], s[44:45], 0, v[166:167]
	s_add_u32 s46, s44, 0x20100
	v_lshl_add_u64 v[176:177], v[174:175], 0, s[48:49]
	s_mov_b32 m0, s57
	s_addc_u32 s47, s45, 0
	global_load_lds_dwordx4 v[176:177], off
	v_lshl_add_u64 v[176:177], s[46:47], 0, v[0:1]
	s_mov_b32 m0, s58
	s_nop 0
	global_load_lds_dwordx4 v[176:177], off
	v_lshl_add_u64 v[176:177], s[46:47], 0, v[166:167]
	s_mov_b32 m0, s59
	s_nop 0
	global_load_lds_dwordx4 v[176:177], off
	v_lshl_add_u64 v[176:177], s[42:43], 0, v[162:163]
	v_lshl_add_u64 v[178:179], v[176:177], 0, s[48:49]
	s_mov_b32 m0, s37
	s_nop 0
	global_load_lds_dwordx4 v[178:179], off
	v_lshl_add_u64 v[178:179], s[42:43], 0, v[164:165]
	v_lshl_add_u64 v[232:233], v[178:179], 0, s[48:49]
	s_mov_b32 m0, s60
	s_nop 0
	global_load_lds_dwordx4 v[232:233], off
	s_cmp_eq_u32 s26, 0
	s_cbranch_scc1 .Lrw_first_g2_1
	s_waitcnt vmcnt(24)
	s_branch .Lrw_done_g2_1

.Lrw_done_g2_1:
	s_waitcnt lgkmcnt(0)
	s_barrier
	s_setprio 1
	s_waitcnt lgkmcnt(0)
	v_mfma_scale_f32_16x16x128_f8f6f4 v[94:97], v[18:25], v[198:205], 0, v234, v238 op_sel_hi:[0,0,0]
	v_mfma_scale_f32_16x16x128_f8f6f4 v[90:93], v[26:33], v[198:205], 0, v234, v238 op_sel_hi:[0,0,0]
	s_setprio 0
	s_setprio 1
	v_mfma_scale_f32_16x16x128_f8f6f4 v[86:89], v[18:25], v[206:213], 0, v234, v238 op_sel_hi:[0,0,0]
	v_mfma_scale_f32_16x16x128_f8f6f4 v[82:85], v[26:33], v[206:213], 0, v234, v238 op_sel_hi:[0,0,0]
	s_setprio 0
	s_setprio 1
	v_mfma_scale_f32_16x16x128_f8f6f4 v[78:81], v[18:25], v[216:223], 0, v234, v238 op_sel_hi:[0,0,0]
	v_mfma_scale_f32_16x16x128_f8f6f4 v[74:77], v[26:33], v[216:223], 0, v234, v238 op_sel_hi:[0,0,0]
	s_setprio 0
	s_setprio 1
	v_mfma_scale_f32_16x16x128_f8f6f4 v[70:73], v[18:25], v[224:231], 0, v234, v238 op_sel_hi:[0,0,0]
	v_mfma_scale_f32_16x16x128_f8f6f4 v[66:69], v[26:33], v[224:231], 0, v234, v238 op_sel_hi:[0,0,0]
	s_setprio 0
	s_setprio 1
	v_mfma_scale_f32_16x16x128_f8f6f4 v[62:65], v[2:9], v[198:205], 0, v234, v238 op_sel_hi:[0,0,0]
	v_mfma_scale_f32_16x16x128_f8f6f4 v[58:61], v[10:17], v[198:205], 0, v234, v238 op_sel_hi:[0,0,0]
	s_setprio 0
	s_setprio 1
	v_mfma_scale_f32_16x16x128_f8f6f4 v[54:57], v[2:9], v[206:213], 0, v234, v238 op_sel_hi:[0,0,0]
	v_mfma_scale_f32_16x16x128_f8f6f4 v[50:53], v[10:17], v[206:213], 0, v234, v238 op_sel_hi:[0,0,0]
	s_setprio 0
	s_setprio 1
	v_mfma_scale_f32_16x16x128_f8f6f4 v[46:49], v[2:9], v[216:223], 0, v234, v238 op_sel_hi:[0,0,0]
	v_mfma_scale_f32_16x16x128_f8f6f4 v[42:45], v[10:17], v[216:223], 0, v234, v238 op_sel_hi:[0,0,0]
	s_setprio 0
	s_setprio 1
	v_mfma_scale_f32_16x16x128_f8f6f4 v[38:41], v[2:9], v[224:231], 0, v234, v238 op_sel_hi:[0,0,0]
	v_mfma_scale_f32_16x16x128_f8f6f4 v[34:37], v[10:17], v[224:231], 0, v234, v238 op_sel_hi:[0,0,0]
	s_setprio 0
	s_barrier
	ds_read_b128 v[18:21], v188
	ds_read_b128 v[22:25], v189
	ds_read_b128 v[26:29], v190
	ds_read_b128 v[30:33], v191
	ds_read_b128 v[2:5], v192
	ds_read_b128 v[6:9], v193
	ds_read_b128 v[10:13], v194
	ds_read_b128 v[14:17], v195
	s_add_u32 s46, s42, 0x20100
	s_addc_u32 s47, s43, 0
	s_mov_b32 m0, s61
	v_lshl_add_u64 v[232:233], s[46:47], 0, v[162:163]
	ds_read_b128 v[198:201], v196 offset:32768
	ds_read_b128 v[202:205], v196 offset:33792
	ds_read_b128 v[206:209], v196 offset:34816
	ds_read_b128 v[210:213], v196 offset:35840
	ds_read_b128 v[216:219], v196 offset:36864
	ds_read_b128 v[220:223], v196 offset:37888
	ds_read_b128 v[224:227], v196 offset:38912
	ds_read_b128 v[228:231], v196 offset:39936
	global_load_lds_dwordx4 v[232:233], off
	v_lshl_add_u64 v[232:233], s[46:47], 0, v[164:165]
	s_mov_b32 m0, s62
	s_nop 0
	global_load_lds_dwordx4 v[232:233], off
	s_waitcnt vmcnt(8)
	s_waitcnt lgkmcnt(0)
	s_barrier
	s_setprio 1
	s_waitcnt lgkmcnt(0)
	v_mfma_scale_f32_16x16x128_f8f6f4 v[158:161], v[18:25], v[198:205], v[158:161], v234, v238 op_sel_hi:[0,0,0]
	v_mfma_scale_f32_16x16x128_f8f6f4 v[154:157], v[26:33], v[198:205], v[154:157], v234, v238 op_sel_hi:[0,0,0]
	s_setprio 0
	s_setprio 1
	v_mfma_scale_f32_16x16x128_f8f6f4 v[150:153], v[18:25], v[206:213], v[150:153], v234, v238 op_sel_hi:[0,0,0]
	v_mfma_scale_f32_16x16x128_f8f6f4 v[146:149], v[26:33], v[206:213], v[146:149], v234, v238 op_sel_hi:[0,0,0]
	s_setprio 0
	s_setprio 1
	v_mfma_scale_f32_16x16x128_f8f6f4 v[142:145], v[18:25], v[216:223], v[142:145], v234, v238 op_sel_hi:[0,0,0]
	v_mfma_scale_f32_16x16x128_f8f6f4 v[138:141], v[26:33], v[216:223], v[138:141], v234, v238 op_sel_hi:[0,0,0]
	s_setprio 0
	s_setprio 1
	v_mfma_scale_f32_16x16x128_f8f6f4 v[134:137], v[18:25], v[224:231], v[134:137], v234, v238 op_sel_hi:[0,0,0]
	v_mfma_scale_f32_16x16x128_f8f6f4 v[130:133], v[26:33], v[224:231], v[130:133], v234, v238 op_sel_hi:[0,0,0]
	s_setprio 0
	s_setprio 1
	v_mfma_scale_f32_16x16x128_f8f6f4 v[126:129], v[2:9], v[198:205], v[126:129], v234, v238 op_sel_hi:[0,0,0]
	v_mfma_scale_f32_16x16x128_f8f6f4 v[122:125], v[10:17], v[198:205], v[122:125], v234, v238 op_sel_hi:[0,0,0]
	s_setprio 0
	s_setprio 1
	v_mfma_scale_f32_16x16x128_f8f6f4 v[118:121], v[2:9], v[206:213], v[118:121], v234, v238 op_sel_hi:[0,0,0]
	v_mfma_scale_f32_16x16x128_f8f6f4 v[114:117], v[10:17], v[206:213], v[114:117], v234, v238 op_sel_hi:[0,0,0]
	s_setprio 0
	s_setprio 1
	v_mfma_scale_f32_16x16x128_f8f6f4 v[110:113], v[2:9], v[216:223], v[110:113], v234, v238 op_sel_hi:[0,0,0]
	v_mfma_scale_f32_16x16x128_f8f6f4 v[106:109], v[10:17], v[216:223], v[106:109], v234, v238 op_sel_hi:[0,0,0]
	s_setprio 0
	s_setprio 1
	v_mfma_scale_f32_16x16x128_f8f6f4 v[102:105], v[2:9], v[224:231], v[102:105], v234, v238 op_sel_hi:[0,0,0]
	v_mfma_scale_f32_16x16x128_f8f6f4 v[98:101], v[10:17], v[224:231], v[98:101], v234, v238 op_sel_hi:[0,0,0]
	s_setprio 0
	s_barrier
	s_mov_b64 s[48:49], 0x180
	s_mov_b32 m0, s65
	v_lshl_add_u64 v[172:173], v[172:173], 0, s[48:49]
	s_add_u32 s46, s44, 0x20180
	ds_read_b128 v[198:201], v196 offset:49152
	ds_read_b128 v[202:205], v196 offset:50176
	ds_read_b128 v[206:209], v196 offset:51200
	ds_read_b128 v[210:213], v196 offset:52224
	ds_read_b128 v[216:219], v196 offset:53248
	ds_read_b128 v[220:223], v196 offset:54272
	ds_read_b128 v[224:227], v196 offset:55296
	ds_read_b128 v[228:231], v196 offset:56320
	global_load_lds_dwordx4 v[172:173], off
	v_lshl_add_u64 v[172:173], v[174:175], 0, s[48:49]
	s_mov_b32 m0, s68
	s_addc_u32 s47, s45, 0
	global_load_lds_dwordx4 v[172:173], off
	v_lshl_add_u64 v[172:173], s[46:47], 0, v[0:1]
	s_mov_b32 m0, s51
	s_nop 0
	global_load_lds_dwordx4 v[172:173], off
	v_lshl_add_u64 v[172:173], s[46:47], 0, v[166:167]
	s_mov_b32 m0, s4
	s_nop 0
	global_load_lds_dwordx4 v[172:173], off
	v_lshl_add_u64 v[172:173], v[176:177], 0, s[48:49]
	s_mov_b32 m0, s81
	s_nop 0
	global_load_lds_dwordx4 v[172:173], off
	v_lshl_add_u64 v[172:173], v[178:179], 0, s[48:49]
	s_mov_b32 m0, s50
	s_nop 0
	global_load_lds_dwordx4 v[172:173], off
	s_waitcnt vmcnt(8)
	s_waitcnt lgkmcnt(0)
	s_barrier
	s_setprio 1
	s_waitcnt lgkmcnt(0)
	v_mfma_scale_f32_16x16x128_f8f6f4 v[94:97], v[18:25], v[198:205], v[94:97], v234, v238 op_sel_hi:[0,0,0]
	v_mfma_scale_f32_16x16x128_f8f6f4 v[90:93], v[26:33], v[198:205], v[90:93], v234, v238 op_sel_hi:[0,0,0]
	s_setprio 0
	s_setprio 1
	v_mfma_scale_f32_16x16x128_f8f6f4 v[86:89], v[18:25], v[206:213], v[86:89], v234, v238 op_sel_hi:[0,0,0]
	v_mfma_scale_f32_16x16x128_f8f6f4 v[82:85], v[26:33], v[206:213], v[82:85], v234, v238 op_sel_hi:[0,0,0]
	s_setprio 0
	s_setprio 1
	v_mfma_scale_f32_16x16x128_f8f6f4 v[78:81], v[18:25], v[216:223], v[78:81], v234, v238 op_sel_hi:[0,0,0]
	v_mfma_scale_f32_16x16x128_f8f6f4 v[74:77], v[26:33], v[216:223], v[74:77], v234, v238 op_sel_hi:[0,0,0]
	s_setprio 0
	s_setprio 1
	v_mfma_scale_f32_16x16x128_f8f6f4 v[70:73], v[18:25], v[224:231], v[70:73], v234, v238 op_sel_hi:[0,0,0]
	v_mfma_scale_f32_16x16x128_f8f6f4 v[66:69], v[26:33], v[224:231], v[66:69], v234, v238 op_sel_hi:[0,0,0]
	s_setprio 0
	s_setprio 1
	v_mfma_scale_f32_16x16x128_f8f6f4 v[62:65], v[2:9], v[198:205], v[62:65], v234, v238 op_sel_hi:[0,0,0]
	v_mfma_scale_f32_16x16x128_f8f6f4 v[58:61], v[10:17], v[198:205], v[58:61], v234, v238 op_sel_hi:[0,0,0]
	s_setprio 0
	s_setprio 1
	v_mfma_scale_f32_16x16x128_f8f6f4 v[54:57], v[2:9], v[206:213], v[54:57], v234, v238 op_sel_hi:[0,0,0]
	v_mfma_scale_f32_16x16x128_f8f6f4 v[50:53], v[10:17], v[206:213], v[50:53], v234, v238 op_sel_hi:[0,0,0]
	s_setprio 0
	s_setprio 1
	v_mfma_scale_f32_16x16x128_f8f6f4 v[46:49], v[2:9], v[216:223], v[46:49], v234, v238 op_sel_hi:[0,0,0]
	v_mfma_scale_f32_16x16x128_f8f6f4 v[42:45], v[10:17], v[216:223], v[42:45], v234, v238 op_sel_hi:[0,0,0]
	s_setprio 0
	s_setprio 1
	v_mfma_scale_f32_16x16x128_f8f6f4 v[38:41], v[2:9], v[224:231], v[38:41], v234, v238 op_sel_hi:[0,0,0]
	v_mfma_scale_f32_16x16x128_f8f6f4 v[34:37], v[10:17], v[224:231], v[34:37], v234, v238 op_sel_hi:[0,0,0]
	s_setprio 0
	s_barrier
	s_add_u32 s42, s42, 0x20180
	s_addc_u32 s43, s43, 0
	s_add_u32 s48, s44, 0x200
	s_addc_u32 s49, s45, 0
	s_mov_b32 s74, 0
.LBB0_2089:
	ds_read_b128 v[2:5], v180
	ds_read_b128 v[6:9], v181
	ds_read_b128 v[10:13], v182
	ds_read_b128 v[14:17], v183
	ds_read_b128 v[26:29], v184
	ds_read_b128 v[30:33], v185
	ds_read_b128 v[172:175], v186
	ds_read_b128 v[176:179], v187
	s_add_u32 s44, s42, 0xfffe0080
	s_addc_u32 s45, s43, -1
	s_cmp_eq_u32 s74, 4
	s_cselect_b32 s47, s13, s45
	s_cselect_b32 s46, s27, s44
	s_cselect_b32 s45, s35, s49
	s_cselect_b32 s44, s34, s48
	s_mov_b32 m0, s29
	v_lshl_add_u64 v[224:225], s[42:43], 0, v[168:169]
	ds_read_b128 v[18:21], v196
	ds_read_b128 v[22:25], v196 offset:1024
	ds_read_b128 v[198:201], v196 offset:2048
	ds_read_b128 v[202:205], v196 offset:3072
	ds_read_b128 v[206:209], v196 offset:4096
	ds_read_b128 v[210:213], v196 offset:5120
	ds_read_b128 v[216:219], v196 offset:6144
	ds_read_b128 v[220:223], v196 offset:7168
	global_load_lds_dwordx4 v[224:225], off
	v_lshl_add_u64 v[224:225], s[42:43], 0, v[170:171]
	s_mov_b32 m0, s31
	s_nop 0
	global_load_lds_dwordx4 v[224:225], off
	s_waitcnt vmcnt(8)
	s_waitcnt lgkmcnt(0)
	s_barrier
	s_setprio 1
	s_waitcnt lgkmcnt(0)
	v_mfma_scale_f32_16x16x128_f8f6f4 v[158:161], v[2:9], v[18:25], v[158:161], v234, v238 op_sel_hi:[0,0,0]
	v_mfma_scale_f32_16x16x128_f8f6f4 v[154:157], v[10:17], v[18:25], v[154:157], v234, v238 op_sel_hi:[0,0,0]
	s_setprio 0
	s_setprio 1
	v_mfma_scale_f32_16x16x128_f8f6f4 v[150:153], v[2:9], v[198:205], v[150:153], v234, v238 op_sel_hi:[0,0,0]
	v_mfma_scale_f32_16x16x128_f8f6f4 v[146:149], v[10:17], v[198:205], v[146:149], v234, v238 op_sel_hi:[0,0,0]
	s_setprio 0
	s_setprio 1
	v_mfma_scale_f32_16x16x128_f8f6f4 v[142:145], v[2:9], v[206:213], v[142:145], v234, v238 op_sel_hi:[0,0,0]
	v_mfma_scale_f32_16x16x128_f8f6f4 v[138:141], v[10:17], v[206:213], v[138:141], v234, v238 op_sel_hi:[0,0,0]
	s_setprio 0
	s_setprio 1
	v_mfma_scale_f32_16x16x128_f8f6f4 v[134:137], v[2:9], v[216:223], v[134:137], v234, v238 op_sel_hi:[0,0,0]
	v_mfma_scale_f32_16x16x128_f8f6f4 v[130:133], v[10:17], v[216:223], v[130:133], v234, v238 op_sel_hi:[0,0,0]
	s_setprio 0
	s_setprio 1
	v_mfma_scale_f32_16x16x128_f8f6f4 v[126:129], v[26:33], v[18:25], v[126:129], v234, v238 op_sel_hi:[0,0,0]
	v_mfma_scale_f32_16x16x128_f8f6f4 v[122:125], v[172:179], v[18:25], v[122:125], v234, v238 op_sel_hi:[0,0,0]
	s_setprio 0
	s_setprio 1
	v_mfma_scale_f32_16x16x128_f8f6f4 v[118:121], v[26:33], v[198:205], v[118:121], v234, v238 op_sel_hi:[0,0,0]
	v_mfma_scale_f32_16x16x128_f8f6f4 v[114:117], v[172:179], v[198:205], v[114:117], v234, v238 op_sel_hi:[0,0,0]
	s_setprio 0
	s_setprio 1
	v_mfma_scale_f32_16x16x128_f8f6f4 v[110:113], v[26:33], v[206:213], v[110:113], v234, v238 op_sel_hi:[0,0,0]
	v_mfma_scale_f32_16x16x128_f8f6f4 v[106:109], v[172:179], v[206:213], v[106:109], v234, v238 op_sel_hi:[0,0,0]
	s_setprio 0
	s_setprio 1
	v_mfma_scale_f32_16x16x128_f8f6f4 v[102:105], v[26:33], v[216:223], v[102:105], v234, v238 op_sel_hi:[0,0,0]
	v_mfma_scale_f32_16x16x128_f8f6f4 v[98:101], v[172:179], v[216:223], v[98:101], v234, v238 op_sel_hi:[0,0,0]
	s_setprio 0
	s_barrier
	s_mov_b32 m0, s41
	v_lshl_add_u64 v[18:19], s[44:45], 0, v[0:1]
	s_add_u32 vcc_lo, s44, 0x20000
	ds_read_b128 v[198:201], v196 offset:16384
	ds_read_b128 v[202:205], v196 offset:17408
	ds_read_b128 v[206:209], v196 offset:18432
	ds_read_b128 v[210:213], v196 offset:19456
	ds_read_b128 v[216:219], v196 offset:20480
	ds_read_b128 v[220:223], v196 offset:21504
	ds_read_b128 v[224:227], v196 offset:22528
	ds_read_b128 v[228:231], v196 offset:23552
	global_load_lds_dwordx4 v[18:19], off
	v_lshl_add_u64 v[20:21], s[44:45], 0, v[166:167]
	s_mov_b32 m0, s57
	s_addc_u32 vcc_hi, s45, 0
	global_load_lds_dwordx4 v[20:21], off
	v_lshl_add_u64 v[22:23], vcc, 0, v[0:1]
	s_mov_b32 m0, s58
	v_lshl_add_u64 v[24:25], s[46:47], 0, v[164:165]
	global_load_lds_dwordx4 v[22:23], off
	v_lshl_add_u64 v[22:23], vcc, 0, v[166:167]
	s_mov_b32 m0, s59
	s_nop 0
	global_load_lds_dwordx4 v[22:23], off
	v_lshl_add_u64 v[22:23], s[46:47], 0, v[162:163]
	s_mov_b32 m0, s37
	s_nop 0
	global_load_lds_dwordx4 v[22:23], off
	s_mov_b32 m0, s60
	s_nop 0
	global_load_lds_dwordx4 v[24:25], off
	s_waitcnt vmcnt(8)
	s_waitcnt lgkmcnt(0)
	s_barrier
	s_setprio 1
	s_waitcnt lgkmcnt(0)
	v_mfma_scale_f32_16x16x128_f8f6f4 v[94:97], v[2:9], v[198:205], v[94:97], v234, v238 op_sel_hi:[0,0,0]
	v_mfma_scale_f32_16x16x128_f8f6f4 v[90:93], v[10:17], v[198:205], v[90:93], v234, v238 op_sel_hi:[0,0,0]
	s_setprio 0
	s_setprio 1
	v_mfma_scale_f32_16x16x128_f8f6f4 v[86:89], v[2:9], v[206:213], v[86:89], v234, v238 op_sel_hi:[0,0,0]
	v_mfma_scale_f32_16x16x128_f8f6f4 v[82:85], v[10:17], v[206:213], v[82:85], v234, v238 op_sel_hi:[0,0,0]
	s_setprio 0
	s_setprio 1
	v_mfma_scale_f32_16x16x128_f8f6f4 v[78:81], v[2:9], v[216:223], v[78:81], v234, v238 op_sel_hi:[0,0,0]
	v_mfma_scale_f32_16x16x128_f8f6f4 v[74:77], v[10:17], v[216:223], v[74:77], v234, v238 op_sel_hi:[0,0,0]
	s_setprio 0
	s_setprio 1
	v_mfma_scale_f32_16x16x128_f8f6f4 v[70:73], v[2:9], v[224:231], v[70:73], v234, v238 op_sel_hi:[0,0,0]
	v_mfma_scale_f32_16x16x128_f8f6f4 v[66:69], v[10:17], v[224:231], v[66:69], v234, v238 op_sel_hi:[0,0,0]
	s_setprio 0
	s_setprio 1
	v_mfma_scale_f32_16x16x128_f8f6f4 v[62:65], v[26:33], v[198:205], v[62:65], v234, v238 op_sel_hi:[0,0,0]
	v_mfma_scale_f32_16x16x128_f8f6f4 v[58:61], v[172:179], v[198:205], v[58:61], v234, v238 op_sel_hi:[0,0,0]
	s_setprio 0
	s_setprio 1
	v_mfma_scale_f32_16x16x128_f8f6f4 v[54:57], v[26:33], v[206:213], v[54:57], v234, v238 op_sel_hi:[0,0,0]
	v_mfma_scale_f32_16x16x128_f8f6f4 v[50:53], v[172:179], v[206:213], v[50:53], v234, v238 op_sel_hi:[0,0,0]
	s_setprio 0
	s_setprio 1
	v_mfma_scale_f32_16x16x128_f8f6f4 v[46:49], v[26:33], v[216:223], v[46:49], v234, v238 op_sel_hi:[0,0,0]
	v_mfma_scale_f32_16x16x128_f8f6f4 v[42:45], v[172:179], v[216:223], v[42:45], v234, v238 op_sel_hi:[0,0,0]
	s_setprio 0
	s_setprio 1
	v_mfma_scale_f32_16x16x128_f8f6f4 v[38:41], v[26:33], v[224:231], v[38:41], v234, v238 op_sel_hi:[0,0,0]
	v_mfma_scale_f32_16x16x128_f8f6f4 v[34:37], v[172:179], v[224:231], v[34:37], v234, v238 op_sel_hi:[0,0,0]
	s_setprio 0
	s_barrier
	ds_read_b128 v[10:13], v188
	ds_read_b128 v[14:17], v189
	ds_read_b128 v[26:29], v190
	ds_read_b128 v[30:33], v191
	ds_read_b128 v[2:5], v192
	ds_read_b128 v[6:9], v193
	ds_read_b128 v[172:175], v194
	ds_read_b128 v[176:179], v195
	s_add_u32 s46, s46, 0x20000
	s_addc_u32 s47, s47, 0
	s_mov_b32 m0, s61
	v_lshl_add_u64 v[232:233], s[46:47], 0, v[162:163]
	ds_read_b128 v[198:201], v196 offset:32768
	ds_read_b128 v[202:205], v196 offset:33792
	ds_read_b128 v[206:209], v196 offset:34816
	ds_read_b128 v[210:213], v196 offset:35840
	ds_read_b128 v[216:219], v196 offset:36864
	ds_read_b128 v[220:223], v196 offset:37888
	ds_read_b128 v[224:227], v196 offset:38912
	ds_read_b128 v[228:231], v196 offset:39936
	global_load_lds_dwordx4 v[232:233], off
	v_lshl_add_u64 v[232:233], s[46:47], 0, v[164:165]
	s_mov_b32 m0, s62
	s_nop 0
	global_load_lds_dwordx4 v[232:233], off
	s_waitcnt vmcnt(8)
	s_waitcnt lgkmcnt(0)
	s_barrier
	s_setprio 1
	s_waitcnt lgkmcnt(0)
	v_mfma_scale_f32_16x16x128_f8f6f4 v[158:161], v[10:17], v[198:205], v[158:161], v234, v238 op_sel_hi:[0,0,0]
	v_mfma_scale_f32_16x16x128_f8f6f4 v[154:157], v[26:33], v[198:205], v[154:157], v234, v238 op_sel_hi:[0,0,0]
	s_setprio 0
	s_setprio 1
	v_mfma_scale_f32_16x16x128_f8f6f4 v[150:153], v[10:17], v[206:213], v[150:153], v234, v238 op_sel_hi:[0,0,0]
	v_mfma_scale_f32_16x16x128_f8f6f4 v[146:149], v[26:33], v[206:213], v[146:149], v234, v238 op_sel_hi:[0,0,0]
	s_setprio 0
	s_setprio 1
	v_mfma_scale_f32_16x16x128_f8f6f4 v[142:145], v[10:17], v[216:223], v[142:145], v234, v238 op_sel_hi:[0,0,0]
	v_mfma_scale_f32_16x16x128_f8f6f4 v[138:141], v[26:33], v[216:223], v[138:141], v234, v238 op_sel_hi:[0,0,0]
	s_setprio 0
	s_setprio 1
	v_mfma_scale_f32_16x16x128_f8f6f4 v[134:137], v[10:17], v[224:231], v[134:137], v234, v238 op_sel_hi:[0,0,0]
	v_mfma_scale_f32_16x16x128_f8f6f4 v[130:133], v[26:33], v[224:231], v[130:133], v234, v238 op_sel_hi:[0,0,0]
	s_setprio 0
	s_setprio 1
	v_mfma_scale_f32_16x16x128_f8f6f4 v[126:129], v[2:9], v[198:205], v[126:129], v234, v238 op_sel_hi:[0,0,0]
	v_mfma_scale_f32_16x16x128_f8f6f4 v[122:125], v[172:179], v[198:205], v[122:125], v234, v238 op_sel_hi:[0,0,0]
	s_setprio 0
	s_setprio 1
	v_mfma_scale_f32_16x16x128_f8f6f4 v[118:121], v[2:9], v[206:213], v[118:121], v234, v238 op_sel_hi:[0,0,0]
	v_mfma_scale_f32_16x16x128_f8f6f4 v[114:117], v[172:179], v[206:213], v[114:117], v234, v238 op_sel_hi:[0,0,0]
	s_setprio 0
	s_setprio 1
	v_mfma_scale_f32_16x16x128_f8f6f4 v[110:113], v[2:9], v[216:223], v[110:113], v234, v238 op_sel_hi:[0,0,0]
	v_mfma_scale_f32_16x16x128_f8f6f4 v[106:109], v[172:179], v[216:223], v[106:109], v234, v238 op_sel_hi:[0,0,0]
	s_setprio 0
	s_setprio 1
	v_mfma_scale_f32_16x16x128_f8f6f4 v[102:105], v[2:9], v[224:231], v[102:105], v234, v238 op_sel_hi:[0,0,0]
	v_mfma_scale_f32_16x16x128_f8f6f4 v[98:101], v[172:179], v[224:231], v[98:101], v234, v238 op_sel_hi:[0,0,0]
	s_setprio 0
	s_barrier
	s_mov_b32 m0, s65
	v_lshl_add_u64 v[18:19], v[18:19], 0, s[66:67]
	s_add_u32 s44, s44, 0x20080
	ds_read_b128 v[198:201], v196 offset:49152
	ds_read_b128 v[202:205], v196 offset:50176
	ds_read_b128 v[206:209], v196 offset:51200
	ds_read_b128 v[210:213], v196 offset:52224
	ds_read_b128 v[216:219], v196 offset:53248
	ds_read_b128 v[220:223], v196 offset:54272
	ds_read_b128 v[224:227], v196 offset:55296
	ds_read_b128 v[228:231], v196 offset:56320
	global_load_lds_dwordx4 v[18:19], off
	v_lshl_add_u64 v[18:19], v[20:21], 0, s[66:67]
	s_mov_b32 m0, s68
	s_addc_u32 s45, s45, 0
	global_load_lds_dwordx4 v[18:19], off
	v_lshl_add_u64 v[18:19], s[44:45], 0, v[0:1]
	s_mov_b32 m0, s51
	s_nop 0
	global_load_lds_dwordx4 v[18:19], off
	v_lshl_add_u64 v[18:19], s[44:45], 0, v[166:167]
	s_mov_b32 m0, s4
	s_nop 0
	global_load_lds_dwordx4 v[18:19], off
	v_lshl_add_u64 v[18:19], v[22:23], 0, s[66:67]
	s_mov_b32 m0, s81
	s_nop 0
	global_load_lds_dwordx4 v[18:19], off
	v_lshl_add_u64 v[18:19], v[24:25], 0, s[66:67]
	s_mov_b32 m0, s50
	s_nop 0
	global_load_lds_dwordx4 v[18:19], off
	s_waitcnt vmcnt(8)
	s_waitcnt lgkmcnt(0)
	s_barrier
	s_setprio 1
	s_waitcnt lgkmcnt(0)
	v_mfma_scale_f32_16x16x128_f8f6f4 v[94:97], v[10:17], v[198:205], v[94:97], v234, v238 op_sel_hi:[0,0,0]
	v_mfma_scale_f32_16x16x128_f8f6f4 v[90:93], v[26:33], v[198:205], v[90:93], v234, v238 op_sel_hi:[0,0,0]
	s_setprio 0
	s_setprio 1
	v_mfma_scale_f32_16x16x128_f8f6f4 v[86:89], v[10:17], v[206:213], v[86:89], v234, v238 op_sel_hi:[0,0,0]
	v_mfma_scale_f32_16x16x128_f8f6f4 v[82:85], v[26:33], v[206:213], v[82:85], v234, v238 op_sel_hi:[0,0,0]
	s_setprio 0
	s_setprio 1
	v_mfma_scale_f32_16x16x128_f8f6f4 v[78:81], v[10:17], v[216:223], v[78:81], v234, v238 op_sel_hi:[0,0,0]
	v_mfma_scale_f32_16x16x128_f8f6f4 v[74:77], v[26:33], v[216:223], v[74:77], v234, v238 op_sel_hi:[0,0,0]
	s_setprio 0
	s_setprio 1
	v_mfma_scale_f32_16x16x128_f8f6f4 v[70:73], v[10:17], v[224:231], v[70:73], v234, v238 op_sel_hi:[0,0,0]
	v_mfma_scale_f32_16x16x128_f8f6f4 v[66:69], v[26:33], v[224:231], v[66:69], v234, v238 op_sel_hi:[0,0,0]
	s_setprio 0
	s_setprio 1
	v_mfma_scale_f32_16x16x128_f8f6f4 v[62:65], v[2:9], v[198:205], v[62:65], v234, v238 op_sel_hi:[0,0,0]
	v_mfma_scale_f32_16x16x128_f8f6f4 v[58:61], v[172:179], v[198:205], v[58:61], v234, v238 op_sel_hi:[0,0,0]
	s_setprio 0
	s_setprio 1
	v_mfma_scale_f32_16x16x128_f8f6f4 v[54:57], v[2:9], v[206:213], v[54:57], v234, v238 op_sel_hi:[0,0,0]
	v_mfma_scale_f32_16x16x128_f8f6f4 v[50:53], v[172:179], v[206:213], v[50:53], v234, v238 op_sel_hi:[0,0,0]
	s_setprio 0
	s_setprio 1
	v_mfma_scale_f32_16x16x128_f8f6f4 v[46:49], v[2:9], v[216:223], v[46:49], v234, v238 op_sel_hi:[0,0,0]
	v_mfma_scale_f32_16x16x128_f8f6f4 v[42:45], v[172:179], v[216:223], v[42:45], v234, v238 op_sel_hi:[0,0,0]
	s_setprio 0
	s_setprio 1
	v_mfma_scale_f32_16x16x128_f8f6f4 v[38:41], v[2:9], v[224:231], v[38:41], v234, v238 op_sel_hi:[0,0,0]
	v_mfma_scale_f32_16x16x128_f8f6f4 v[34:37], v[172:179], v[224:231], v[34:37], v234, v238 op_sel_hi:[0,0,0]
	s_setprio 0
	s_barrier
	s_add_i32 s74, s74, 2
	s_add_u32 s42, s42, 0x100
	s_addc_u32 s43, s43, 0
	s_add_u32 s48, s48, 0x100
	s_addc_u32 s49, s49, 0
	s_cmp_gt_u32 s74, 5
	s_cbranch_scc0 .LBB0_2089
	s_and_b64 vcc, exec, s[8:9]
	s_cbranch_vccz .LBB0_2092
	s_barrier
